# plus: in P2/P6/P7/P11 K-loops two of SP2's six LDS-DMA issues deferred into the following MFMA block, SP2 waits vmcnt(6)
# speedup vs baseline: 1.0477x; 1.0477x over previous
; #define PG8_STAGE(bufoff, gbase, voff) do { _Pragma("unroll") for (int _i = 0; _i < 2; ++_i) \
;         __builtin_amdgcn_global_load_lds((const unsigned*)((const char*)(gbase) + (voff)[_i]), (PG8_LAS unsigned*)(lds + (bufoff) + ldsw + _i * 8192), 16, 0, 0); } while (0)
; #define PG8_LDA(dst, b, h) do { _Pragma("unroll") for (int m = 0; m < 4; ++m) _Pragma("unroll") for (int k = 0; k < 2; ++k) dst[m][k] = *(const PG8_LAS bf16x8*)(lds + PG8_SA(b, h) + aoff + m * 2048 + k * 1024); } while (0)
; #define PG8_LDB(dst, b, h) do { _Pragma("unroll") for (int n = 0; n < 2; ++n) _Pragma("unroll") for (int k = 0; k < 2; ++k) dst[n][k] = *(const PG8_LAS bf16x8*)(lds + PG8_SB(b, h) + boff + n * 2048 + k * 1024); } while (0)
; #define PG8_MMA(ai, bj, At, Bt) do { __builtin_amdgcn_s_setprio(1); _Pragma("unroll") for (int m = 0; m < 4; ++m) _Pragma("unroll") for (int n = 0; n < 2; ++n) _Pragma("unroll") for (int k = 0; k < 2; ++k) \
;         acc[ai][bj][m][n] = __builtin_amdgcn_mfma_f32_16x16x32_bf16(Bt[n][k], At[m][k], acc[ai][bj][m][n], 0, 0, 0); __builtin_amdgcn_s_setprio(0); } while (0)
; #define PG8_WAIT_V(n) asm volatile("s_waitcnt vmcnt(" #n ")" ::: "memory")
; #define PG8_WAIT_L(n) asm volatile("s_waitcnt lgkmcnt(" #n ")" ::: "memory")
; #define PG8_BAR __builtin_amdgcn_s_barrier()
; template <class Epi, class Sched, bool ALIGN_EPI = false, bool SP2 = false>
; __device__ __forceinline__ void gemm_phase(PG8_LAS unsigned char* lds, const Gemm g, const Sched& S, const Epi& E) {
;     ...
;             const char* a1 = cA + (size_t)(t + 1) * kstep;
;             const char* a2 = last ? nA : cA + (size_t)(t + 2) * kstep; const char* b2 = last ? nB : cB + (size_t)(t + 2) * kstep;
;             const char* a3 = a2 + kstep; const char* b3 = b2 + kstep;
;             if (last && has_next) S.a_ready(nxt);
;             if constexpr (SP2) {
;             PG8_LDB(B0, 0, 0); PG8_LDB(B1, 0, 1); PG8_SCHED; PG8_LDA(At, 0, 0); PG8_STAGE(PG8_SA(1, 1), a1 + hstep, voffA);
;             PG8_WAIT_V(8); PG8_WAIT_L(0); PG8_BAR; PG8_MMA(0, 0, At, B0); PG8_MMA(0, 1, At, B1); PG8_BAR; PG8_SCHED;
;             PG8_LDA(At, 0, 1); PG8_STAGE(PG8_SB(0, 0), b2, voffB); PG8_STAGE(PG8_SB(0, 1), b2 + hstep, voffB); PG8_STAGE(PG8_SA(0, 0), a2, voffA);
;             PG8_WAIT_V(8); PG8_WAIT_L(0); PG8_BAR; PG8_MMA(1, 0, At, B0); PG8_MMA(1, 1, At, B1); PG8_BAR; PG8_SCHED;
.LBB0_332:
	ds_read_b128 v[132:135], v213
	ds_read_b128 v[136:139], v213 offset:1024
	ds_read_b128 v[140:143], v213 offset:2048
	ds_read_b128 v[144:147], v213 offset:3072
	ds_read_b128 v[148:151], v214
	ds_read_b128 v[152:155], v214 offset:1024
	ds_read_b128 v[156:159], v214 offset:2048
	ds_read_b128 v[178:181], v214 offset:3072
	s_add_u32 s2, s0, 0xfff80080
	s_addc_u32 s3, s1, -1
	s_cmp_eq_u32 s95, 28
	s_cselect_b32 s5, s7, s3
	s_cselect_b32 s4, s33, s2
	s_cselect_b32 s3, s53, s85
	s_cselect_b32 s2, s55, s84
	v_lshl_add_u64 v[160:161], s[0:1], 0, v[172:173]
	s_add_i32 m0, s63, 0xc000
	ds_read_b128 v[182:185], v215
	ds_read_b128 v[188:191], v215 offset:1024
	ds_read_b128 v[192:195], v215 offset:2048
	ds_read_b128 v[196:199], v215 offset:3072
	ds_read_b128 v[200:203], v215 offset:4096
	ds_read_b128 v[204:207], v215 offset:5120
	ds_read_b128 v[218:221], v215 offset:6144
	ds_read_b128 v[222:225], v215 offset:7168
	global_load_lds_dwordx4 v[160:161], off
	v_lshl_add_u64 v[160:161], s[0:1], 0, v[174:175]
	s_add_i32 m0, s63, 0xe000
	s_nop 0
	global_load_lds_dwordx4 v[160:161], off
	s_waitcnt vmcnt(8)
	s_waitcnt lgkmcnt(0)
	s_barrier
	s_setprio 1
	s_waitcnt lgkmcnt(0)
	v_mfma_f32_16x16x32_bf16 v[126:129], v[132:135], v[182:185], v[126:129]
	v_mfma_f32_16x16x32_bf16 v[122:125], v[140:143], v[182:185], v[122:125]
	v_mfma_f32_16x16x32_bf16 v[118:121], v[132:135], v[192:195], v[118:121]
	v_mfma_f32_16x16x32_bf16 v[110:113], v[140:143], v[192:195], v[110:113]
	v_mfma_f32_16x16x32_bf16 v[102:105], v[132:135], v[200:203], v[102:105]
	v_mfma_f32_16x16x32_bf16 v[94:97], v[140:143], v[200:203], v[94:97]
	v_mfma_f32_16x16x32_bf16 v[86:89], v[132:135], v[218:221], v[86:89]
	v_mfma_f32_16x16x32_bf16 v[78:81], v[140:143], v[218:221], v[78:81]
	v_mfma_f32_16x16x32_bf16 v[126:129], v[136:139], v[188:191], v[126:129]
	v_mfma_f32_16x16x32_bf16 v[122:125], v[144:147], v[188:191], v[122:125]
	v_mfma_f32_16x16x32_bf16 v[118:121], v[136:139], v[196:199], v[118:121]
	v_mfma_f32_16x16x32_bf16 v[110:113], v[144:147], v[196:199], v[110:113]
	v_mfma_f32_16x16x32_bf16 v[102:105], v[136:139], v[204:207], v[102:105]
	v_mfma_f32_16x16x32_bf16 v[94:97], v[144:147], v[204:207], v[94:97]
	v_mfma_f32_16x16x32_bf16 v[86:89], v[136:139], v[222:225], v[86:89]
	v_mfma_f32_16x16x32_bf16 v[78:81], v[144:147], v[222:225], v[78:81]
	s_setprio 0
	s_setprio 1
	v_mfma_f32_16x16x32_bf16 v[114:117], v[148:151], v[182:185], v[114:117]
	v_mfma_f32_16x16x32_bf16 v[106:109], v[156:159], v[182:185], v[106:109]
	v_mfma_f32_16x16x32_bf16 v[98:101], v[148:151], v[192:195], v[98:101]
	v_mfma_f32_16x16x32_bf16 v[90:93], v[156:159], v[192:195], v[90:93]
	v_mfma_f32_16x16x32_bf16 v[82:85], v[148:151], v[200:203], v[82:85]
	v_mfma_f32_16x16x32_bf16 v[74:77], v[156:159], v[200:203], v[74:77]
	v_mfma_f32_16x16x32_bf16 v[70:73], v[148:151], v[218:221], v[70:73]
	v_mfma_f32_16x16x32_bf16 v[66:69], v[156:159], v[218:221], v[66:69]
	v_mfma_f32_16x16x32_bf16 v[114:117], v[152:155], v[188:191], v[114:117]
	v_mfma_f32_16x16x32_bf16 v[106:109], v[178:181], v[188:191], v[106:109]
	v_mfma_f32_16x16x32_bf16 v[98:101], v[152:155], v[196:199], v[98:101]
	v_mfma_f32_16x16x32_bf16 v[90:93], v[178:181], v[196:199], v[90:93]
	v_mfma_f32_16x16x32_bf16 v[82:85], v[152:155], v[204:207], v[82:85]
	v_mfma_f32_16x16x32_bf16 v[74:77], v[178:181], v[204:207], v[74:77]
	v_mfma_f32_16x16x32_bf16 v[70:73], v[152:155], v[222:225], v[70:73]
	v_mfma_f32_16x16x32_bf16 v[66:69], v[178:181], v[222:225], v[66:69]
	s_setprio 0
	s_barrier
	s_add_i32 s96, s81, s66
	v_lshl_add_u64 v[160:161], s[2:3], 0, v[164:165]
	s_mov_b32 m0, s96
	ds_read_b128 v[182:185], v215 offset:16384
	ds_read_b128 v[188:191], v215 offset:17408
	ds_read_b128 v[192:195], v215 offset:18432
	ds_read_b128 v[196:199], v215 offset:19456
	ds_read_b128 v[200:203], v215 offset:20480
	ds_read_b128 v[204:207], v215 offset:21504
	ds_read_b128 v[218:221], v215 offset:22528
	ds_read_b128 v[222:225], v215 offset:23552
	global_load_lds_dwordx4 v[160:161], off
	s_add_i32 m0, s96, 0x2000
	s_add_u32 s96, s2, 0x80000
	v_lshl_add_u64 v[208:209], s[2:3], 0, v[168:169]
	s_addc_u32 s97, s3, 0
	s_add_i32 vcc_lo, s82, s66
	global_load_lds_dwordx4 v[208:209], off
	v_lshl_add_u64 v[226:227], s[96:97], 0, v[164:165]
	s_mov_b32 m0, vcc_lo
	v_lshl_add_u64 v[228:229], s[4:5], 0, v[166:167]
	global_load_lds_dwordx4 v[226:227], off
	v_lshl_add_u64 v[226:227], s[96:97], 0, v[168:169]
	s_add_i32 m0, vcc_lo, 0x2000
	s_nop 0
	global_load_lds_dwordx4 v[226:227], off
	v_lshl_add_u64 v[226:227], s[4:5], 0, v[162:163]
	s_waitcnt vmcnt(6)
	s_waitcnt lgkmcnt(0)
	s_barrier
; #define PG8_STAGE(bufoff, gbase, voff) do { _Pragma("unroll") for (int _i = 0; _i < 2; ++_i) \
;         __builtin_amdgcn_global_load_lds((const unsigned*)((const char*)(gbase) + (voff)[_i]), (PG8_LAS unsigned*)(lds + (bufoff) + ldsw + _i * 8192), 16, 0, 0); } while (0)
; #define PG8_LDA(dst, b, h) do { _Pragma("unroll") for (int m = 0; m < 4; ++m) _Pragma("unroll") for (int k = 0; k < 2; ++k) dst[m][k] = *(const PG8_LAS bf16x8*)(lds + PG8_SA(b, h) + aoff + m * 2048 + k * 1024); } while (0)
; #define PG8_LDB(dst, b, h) do { _Pragma("unroll") for (int n = 0; n < 2; ++n) _Pragma("unroll") for (int k = 0; k < 2; ++k) dst[n][k] = *(const PG8_LAS bf16x8*)(lds + PG8_SB(b, h) + boff + n * 2048 + k * 1024); } while (0)
; #define PG8_MMA(ai, bj, At, Bt) do { __builtin_amdgcn_s_setprio(1); _Pragma("unroll") for (int m = 0; m < 4; ++m) _Pragma("unroll") for (int n = 0; n < 2; ++n) _Pragma("unroll") for (int k = 0; k < 2; ++k) \
;         acc[ai][bj][m][n] = __builtin_amdgcn_mfma_f32_16x16x32_bf16(Bt[n][k], At[m][k], acc[ai][bj][m][n], 0, 0, 0); __builtin_amdgcn_s_setprio(0); } while (0)
; #define PG8_WAIT_V(n) asm volatile("s_waitcnt vmcnt(" #n ")" ::: "memory")
; #define PG8_WAIT_L(n) asm volatile("s_waitcnt lgkmcnt(" #n ")" ::: "memory")
; #define PG8_BAR __builtin_amdgcn_s_barrier()
; #define PG8_SCHED __builtin_amdgcn_sched_barrier(0)
; #define PG8_STAGE(bufoff, gbase, voff) do { _Pragma("unroll") for (int _i = 0; _i < 2; ++_i) \
;         __builtin_amdgcn_global_load_lds((const unsigned*)((const char*)(gbase) + (voff)[_i]), (PG8_LAS unsigned*)(lds + (bufoff) + ldsw + _i * 8192), 16, 0, 0); } while (0)
; #define PG8_WAIT_V(n) asm volatile("s_waitcnt vmcnt(" #n ")" ::: "memory")
; #define PG8_WAIT_L(n) asm volatile("s_waitcnt lgkmcnt(" #n ")" ::: "memory")
; #define PG8_BAR __builtin_amdgcn_s_barrier()
; template <class Epi, class Sched, bool ALIGN_EPI = false, bool SP2 = false>
; __device__ __forceinline__ void gemm_phase(PG8_LAS unsigned char* lds, const Gemm g, const Sched& S, const Epi& E) {
;     ...
;             PG8_WAIT_V(8); PG8_WAIT_L(0); PG8_BAR; PG8_MMA(1, 0, At, B0); PG8_MMA(1, 1, At, B1); PG8_BAR; PG8_SCHED;
;             PG8_LDB(B0, 1, 0); PG8_LDB(B1, 1, 1); PG8_SCHED; PG8_LDA(At, 1, 0); PG8_STAGE(PG8_SA(0, 1), a2 + hstep, voffA);
;             PG8_WAIT_V(8); PG8_WAIT_L(0); PG8_BAR; PG8_MMA(0, 0, At, B0); PG8_MMA(0, 1, At, B1); PG8_BAR; PG8_SCHED;
	s_setprio 1
	s_waitcnt lgkmcnt(0)
	v_mfma_f32_16x16x32_bf16 v[62:65], v[132:135], v[182:185], v[62:65]
	v_mfma_f32_16x16x32_bf16 v[58:61], v[140:143], v[182:185], v[58:61]
	v_mfma_f32_16x16x32_bf16 v[54:57], v[132:135], v[192:195], v[54:57]
	v_mfma_f32_16x16x32_bf16 v[46:49], v[140:143], v[192:195], v[46:49]
	v_mfma_f32_16x16x32_bf16 v[38:41], v[132:135], v[200:203], v[38:41]
	v_mfma_f32_16x16x32_bf16 v[30:33], v[140:143], v[200:203], v[30:33]
	v_mfma_f32_16x16x32_bf16 v[22:25], v[132:135], v[218:221], v[22:25]
	v_mfma_f32_16x16x32_bf16 v[14:17], v[140:143], v[218:221], v[14:17]
	v_mfma_f32_16x16x32_bf16 v[62:65], v[136:139], v[188:191], v[62:65]
	v_mfma_f32_16x16x32_bf16 v[58:61], v[144:147], v[188:191], v[58:61]
	v_mfma_f32_16x16x32_bf16 v[54:57], v[136:139], v[196:199], v[54:57]
	v_mfma_f32_16x16x32_bf16 v[46:49], v[144:147], v[196:199], v[46:49]
	v_mfma_f32_16x16x32_bf16 v[38:41], v[136:139], v[204:207], v[38:41]
	v_mfma_f32_16x16x32_bf16 v[30:33], v[144:147], v[204:207], v[30:33]
	v_mfma_f32_16x16x32_bf16 v[22:25], v[136:139], v[222:225], v[22:25]
	v_mfma_f32_16x16x32_bf16 v[14:17], v[144:147], v[222:225], v[14:17]
	s_mov_b32 m0, s63
	s_nop 0
	global_load_lds_dwordx4 v[226:227], off
	s_mov_b32 m0, s65
	s_nop 0
	global_load_lds_dwordx4 v[228:229], off
	s_setprio 0
	s_setprio 1
	v_mfma_f32_16x16x32_bf16 v[50:53], v[148:151], v[182:185], v[50:53]
	v_mfma_f32_16x16x32_bf16 v[42:45], v[156:159], v[182:185], v[42:45]
	v_mfma_f32_16x16x32_bf16 v[34:37], v[148:151], v[192:195], v[34:37]
	v_mfma_f32_16x16x32_bf16 v[26:29], v[156:159], v[192:195], v[26:29]
	v_mfma_f32_16x16x32_bf16 v[18:21], v[148:151], v[200:203], v[18:21]
	v_mfma_f32_16x16x32_bf16 v[10:13], v[156:159], v[200:203], v[10:13]
	v_mfma_f32_16x16x32_bf16 v[6:9], v[148:151], v[218:221], v[6:9]
	v_mfma_f32_16x16x32_bf16 v[2:5], v[156:159], v[218:221], v[2:5]
	v_mfma_f32_16x16x32_bf16 v[50:53], v[152:155], v[188:191], v[50:53]
	v_mfma_f32_16x16x32_bf16 v[42:45], v[178:181], v[188:191], v[42:45]
	v_mfma_f32_16x16x32_bf16 v[34:37], v[152:155], v[196:199], v[34:37]
	v_mfma_f32_16x16x32_bf16 v[26:29], v[178:181], v[196:199], v[26:29]
	v_mfma_f32_16x16x32_bf16 v[18:21], v[152:155], v[204:207], v[18:21]
	v_mfma_f32_16x16x32_bf16 v[10:13], v[178:181], v[204:207], v[10:13]
	v_mfma_f32_16x16x32_bf16 v[6:9], v[152:155], v[222:225], v[6:9]
	v_mfma_f32_16x16x32_bf16 v[2:5], v[178:181], v[222:225], v[2:5]
	s_setprio 0
	s_barrier
	s_add_i32 s96, 0, 0x18000
	v_add_u32_e32 v131, s96, v211
	s_add_i32 s97, 0, 0x1c000
	ds_read_b128 v[132:135], v131
	ds_read_b128 v[136:139], v131 offset:1024
	ds_read_b128 v[140:143], v131 offset:2048
	ds_read_b128 v[144:147], v131 offset:3072
	v_add_u32_e32 v131, s97, v211
	ds_read_b128 v[148:151], v131
	ds_read_b128 v[152:155], v131 offset:1024
	ds_read_b128 v[156:159], v131 offset:2048
	ds_read_b128 v[178:181], v131 offset:3072
	s_add_u32 s4, s4, 0x80000
	s_addc_u32 s5, s5, 0
	s_mov_b32 m0, s71
	v_lshl_add_u64 v[230:231], s[4:5], 0, v[162:163]
	ds_read_b128 v[182:185], v215 offset:32768
	ds_read_b128 v[188:191], v215 offset:33792
	ds_read_b128 v[192:195], v215 offset:34816
	ds_read_b128 v[196:199], v215 offset:35840
	ds_read_b128 v[200:203], v215 offset:36864
	ds_read_b128 v[204:207], v215 offset:37888
	ds_read_b128 v[218:221], v215 offset:38912
	ds_read_b128 v[222:225], v215 offset:39936
	global_load_lds_dwordx4 v[230:231], off
	v_lshl_add_u64 v[230:231], s[4:5], 0, v[166:167]
	s_mov_b32 m0, s72
	s_nop 0
	global_load_lds_dwordx4 v[230:231], off
	s_waitcnt vmcnt(8)
	s_waitcnt lgkmcnt(0)
	s_barrier
	s_setprio 1
	s_waitcnt lgkmcnt(0)
	v_mfma_f32_16x16x32_bf16 v[126:129], v[132:135], v[182:185], v[126:129]
	v_mfma_f32_16x16x32_bf16 v[122:125], v[140:143], v[182:185], v[122:125]
	v_mfma_f32_16x16x32_bf16 v[118:121], v[132:135], v[192:195], v[118:121]
	v_mfma_f32_16x16x32_bf16 v[110:113], v[140:143], v[192:195], v[110:113]
	v_mfma_f32_16x16x32_bf16 v[102:105], v[132:135], v[200:203], v[102:105]
	v_mfma_f32_16x16x32_bf16 v[94:97], v[140:143], v[200:203], v[94:97]
	v_mfma_f32_16x16x32_bf16 v[86:89], v[132:135], v[218:221], v[86:89]
	v_mfma_f32_16x16x32_bf16 v[78:81], v[140:143], v[218:221], v[78:81]
	v_mfma_f32_16x16x32_bf16 v[126:129], v[136:139], v[188:191], v[126:129]
	v_mfma_f32_16x16x32_bf16 v[122:125], v[144:147], v[188:191], v[122:125]
	v_mfma_f32_16x16x32_bf16 v[118:121], v[136:139], v[196:199], v[118:121]
	v_mfma_f32_16x16x32_bf16 v[110:113], v[144:147], v[196:199], v[110:113]
	v_mfma_f32_16x16x32_bf16 v[102:105], v[136:139], v[204:207], v[102:105]
	v_mfma_f32_16x16x32_bf16 v[94:97], v[144:147], v[204:207], v[94:97]
	v_mfma_f32_16x16x32_bf16 v[86:89], v[136:139], v[222:225], v[86:89]
	v_mfma_f32_16x16x32_bf16 v[78:81], v[144:147], v[222:225], v[78:81]
	s_setprio 0
	s_setprio 1
	v_mfma_f32_16x16x32_bf16 v[114:117], v[148:151], v[182:185], v[114:117]
	v_mfma_f32_16x16x32_bf16 v[106:109], v[156:159], v[182:185], v[106:109]
	v_mfma_f32_16x16x32_bf16 v[98:101], v[148:151], v[192:195], v[98:101]
	v_mfma_f32_16x16x32_bf16 v[90:93], v[156:159], v[192:195], v[90:93]
	v_mfma_f32_16x16x32_bf16 v[82:85], v[148:151], v[200:203], v[82:85]
	v_mfma_f32_16x16x32_bf16 v[74:77], v[156:159], v[200:203], v[74:77]
	v_mfma_f32_16x16x32_bf16 v[70:73], v[148:151], v[218:221], v[70:73]
	v_mfma_f32_16x16x32_bf16 v[66:69], v[156:159], v[218:221], v[66:69]
	v_mfma_f32_16x16x32_bf16 v[114:117], v[152:155], v[188:191], v[114:117]
	v_mfma_f32_16x16x32_bf16 v[106:109], v[178:181], v[188:191], v[106:109]
	v_mfma_f32_16x16x32_bf16 v[98:101], v[152:155], v[196:199], v[98:101]
	v_mfma_f32_16x16x32_bf16 v[90:93], v[178:181], v[196:199], v[90:93]
	v_mfma_f32_16x16x32_bf16 v[82:85], v[152:155], v[204:207], v[82:85]
	v_mfma_f32_16x16x32_bf16 v[74:77], v[178:181], v[204:207], v[74:77]
	v_mfma_f32_16x16x32_bf16 v[70:73], v[152:155], v[222:225], v[70:73]
	v_mfma_f32_16x16x32_bf16 v[66:69], v[178:181], v[222:225], v[66:69]
	s_setprio 0
	s_barrier
; #define PG8_STAGE(bufoff, gbase, voff) do { _Pragma("unroll") for (int _i = 0; _i < 2; ++_i) \
;         __builtin_amdgcn_global_load_lds((const unsigned*)((const char*)(gbase) + (voff)[_i]), (PG8_LAS unsigned*)(lds + (bufoff) + ldsw + _i * 8192), 16, 0, 0); } while (0)
; #define PG8_LDA(dst, b, h) do { _Pragma("unroll") for (int m = 0; m < 4; ++m) _Pragma("unroll") for (int k = 0; k < 2; ++k) dst[m][k] = *(const PG8_LAS bf16x8*)(lds + PG8_SA(b, h) + aoff + m * 2048 + k * 1024); } while (0)
; #define PG8_MMA(ai, bj, At, Bt) do { __builtin_amdgcn_s_setprio(1); _Pragma("unroll") for (int m = 0; m < 4; ++m) _Pragma("unroll") for (int n = 0; n < 2; ++n) _Pragma("unroll") for (int k = 0; k < 2; ++k) \
;         acc[ai][bj][m][n] = __builtin_amdgcn_mfma_f32_16x16x32_bf16(Bt[n][k], At[m][k], acc[ai][bj][m][n], 0, 0, 0); __builtin_amdgcn_s_setprio(0); } while (0)
; #define PG8_WAIT_V(n) asm volatile("s_waitcnt vmcnt(" #n ")" ::: "memory")
; #define PG8_WAIT_L(n) asm volatile("s_waitcnt lgkmcnt(" #n ")" ::: "memory")
; #define PG8_BAR __builtin_amdgcn_s_barrier()
; #define PG8_SCHED __builtin_amdgcn_sched_barrier(0)
; #define PG8_STAGE(bufoff, gbase, voff) do { _Pragma("unroll") for (int _i = 0; _i < 2; ++_i) \
;         __builtin_amdgcn_global_load_lds((const unsigned*)((const char*)(gbase) + (voff)[_i]), (PG8_LAS unsigned*)(lds + (bufoff) + ldsw + _i * 8192), 16, 0, 0); } while (0)
; #define PG8_LDA(dst, b, h) do { _Pragma("unroll") for (int m = 0; m < 4; ++m) _Pragma("unroll") for (int k = 0; k < 2; ++k) dst[m][k] = *(const PG8_LAS bf16x8*)(lds + PG8_SA(b, h) + aoff + m * 2048 + k * 1024); } while (0)
; #define PG8_WAIT_V(n) asm volatile("s_waitcnt vmcnt(" #n ")" ::: "memory")
; template <class Epi, class Sched, bool ALIGN_EPI = false, bool SP2 = false>
; __device__ __forceinline__ void gemm_phase(PG8_LAS unsigned char* lds, const Gemm g, const Sched& S, const Epi& E) {
;     ...
;             PG8_LDA(At, 1, 1); PG8_STAGE(PG8_SB(1, 0), b3, voffB); PG8_STAGE(PG8_SB(1, 1), b3 + hstep, voffB); PG8_STAGE(PG8_SA(1, 0), a3, voffA);
;             PG8_WAIT_V(8); PG8_WAIT_L(0); PG8_BAR; PG8_MMA(1, 0, At, B0); PG8_MMA(1, 1, At, B1); PG8_BAR; PG8_SCHED;
;     ...
;         if constexpr (Sched::DYNAMIC) { static_assert(!Sched::DYNAMIC || ALIGN_EPI, "dynamic orders publish in front of the ALIGN_EPI barrier"); S.claim_publish(ui + 2, pend, wid, lane); }
	s_add_i32 s4, s96, s66
	v_lshl_add_u64 v[160:161], v[160:161], 0, s[40:41]
	s_mov_b32 m0, s4
	ds_read_b128 v[182:185], v215 offset:49152
	ds_read_b128 v[188:191], v215 offset:50176
	ds_read_b128 v[192:195], v215 offset:51200
	ds_read_b128 v[196:199], v215 offset:52224
	ds_read_b128 v[200:203], v215 offset:53248
	ds_read_b128 v[204:207], v215 offset:54272
	ds_read_b128 v[218:221], v215 offset:55296
	ds_read_b128 v[222:225], v215 offset:56320
	global_load_lds_dwordx4 v[160:161], off
	s_add_i32 m0, s4, 0x2000
	s_add_u32 s2, s2, 0x80080
	v_lshl_add_u64 v[160:161], v[208:209], 0, s[40:41]
	s_addc_u32 s3, s3, 0
	s_add_i32 s4, s97, s66
	global_load_lds_dwordx4 v[160:161], off
	v_lshl_add_u64 v[160:161], s[2:3], 0, v[164:165]
	s_mov_b32 m0, s4
	s_nop 0
	global_load_lds_dwordx4 v[160:161], off
	v_lshl_add_u64 v[160:161], s[2:3], 0, v[168:169]
	s_add_i32 m0, s4, 0x2000
	s_nop 0
	global_load_lds_dwordx4 v[160:161], off
	v_lshl_add_u64 v[160:161], v[226:227], 0, s[40:41]
	v_lshl_add_u64 v[232:233], v[228:229], 0, s[40:41]
	s_waitcnt vmcnt(6)
	s_waitcnt lgkmcnt(0)
	s_barrier
	s_setprio 1
	s_waitcnt lgkmcnt(0)
	v_mfma_f32_16x16x32_bf16 v[62:65], v[132:135], v[182:185], v[62:65]
	v_mfma_f32_16x16x32_bf16 v[58:61], v[140:143], v[182:185], v[58:61]
	v_mfma_f32_16x16x32_bf16 v[54:57], v[132:135], v[192:195], v[54:57]
	v_mfma_f32_16x16x32_bf16 v[46:49], v[140:143], v[192:195], v[46:49]
	v_mfma_f32_16x16x32_bf16 v[38:41], v[132:135], v[200:203], v[38:41]
	v_mfma_f32_16x16x32_bf16 v[30:33], v[140:143], v[200:203], v[30:33]
	v_mfma_f32_16x16x32_bf16 v[22:25], v[132:135], v[218:221], v[22:25]
	v_mfma_f32_16x16x32_bf16 v[14:17], v[140:143], v[218:221], v[14:17]
	v_mfma_f32_16x16x32_bf16 v[62:65], v[136:139], v[188:191], v[62:65]
	v_mfma_f32_16x16x32_bf16 v[58:61], v[144:147], v[188:191], v[58:61]
	v_mfma_f32_16x16x32_bf16 v[54:57], v[136:139], v[196:199], v[54:57]
	v_mfma_f32_16x16x32_bf16 v[46:49], v[144:147], v[196:199], v[46:49]
	v_mfma_f32_16x16x32_bf16 v[38:41], v[136:139], v[204:207], v[38:41]
	v_mfma_f32_16x16x32_bf16 v[30:33], v[144:147], v[204:207], v[30:33]
	v_mfma_f32_16x16x32_bf16 v[22:25], v[136:139], v[222:225], v[22:25]
	v_mfma_f32_16x16x32_bf16 v[14:17], v[144:147], v[222:225], v[14:17]
	s_mov_b32 m0, s74
	s_nop 0
	global_load_lds_dwordx4 v[160:161], off
	s_mov_b32 m0, s75
	s_nop 0
	global_load_lds_dwordx4 v[232:233], off
	s_setprio 0
	s_setprio 1
	v_mfma_f32_16x16x32_bf16 v[50:53], v[148:151], v[182:185], v[50:53]
	v_mfma_f32_16x16x32_bf16 v[42:45], v[156:159], v[182:185], v[42:45]
	v_mfma_f32_16x16x32_bf16 v[34:37], v[148:151], v[192:195], v[34:37]
	v_mfma_f32_16x16x32_bf16 v[26:29], v[156:159], v[192:195], v[26:29]
	v_mfma_f32_16x16x32_bf16 v[18:21], v[148:151], v[200:203], v[18:21]
	v_mfma_f32_16x16x32_bf16 v[10:13], v[156:159], v[200:203], v[10:13]
	v_mfma_f32_16x16x32_bf16 v[6:9], v[148:151], v[218:221], v[6:9]
	v_mfma_f32_16x16x32_bf16 v[2:5], v[156:159], v[218:221], v[2:5]
	v_mfma_f32_16x16x32_bf16 v[50:53], v[152:155], v[188:191], v[50:53]
	v_mfma_f32_16x16x32_bf16 v[42:45], v[178:181], v[188:191], v[42:45]
	v_mfma_f32_16x16x32_bf16 v[34:37], v[152:155], v[196:199], v[34:37]
	v_mfma_f32_16x16x32_bf16 v[26:29], v[178:181], v[196:199], v[26:29]
	v_mfma_f32_16x16x32_bf16 v[18:21], v[152:155], v[204:207], v[18:21]
	v_mfma_f32_16x16x32_bf16 v[10:13], v[178:181], v[204:207], v[10:13]
	v_mfma_f32_16x16x32_bf16 v[6:9], v[152:155], v[222:225], v[6:9]
	v_mfma_f32_16x16x32_bf16 v[2:5], v[178:181], v[222:225], v[2:5]
	s_setprio 0
	s_barrier
	s_add_i32 s95, s95, 2
	s_add_u32 s0, s0, 0x100
	s_addc_u32 s1, s1, 0
	s_add_u32 s84, s84, 0x100
	s_addc_u32 s85, s85, 0
	s_cmp_gt_u32 s95, 29
	s_cbranch_scc0 .LBB0_332
	s_waitcnt vmcnt(0)
	v_readfirstlane_b32 s2, v130
	s_and_saveexec_b64 s[0:1], s[10:11]
	s_cbranch_execz .LBB0_335
	s_and_b32 s3, s6, 3
	s_xor_b32 s3, s3, 2
	s_and_b64 s[4:5], s[42:43], exec
	s_cselect_b32 s3, s3, s76
	s_lshl_b32 s3, s3, 2
	s_add_i32 s3, s3, 0
	s_add_i32 s3, s3, 0x27da0
	v_mov_b32_e32 v130, s3
	v_mov_b32_e32 v131, s2
	ds_write_b32 v130, v131

; #define PG8_STAGE(bufoff, gbase, voff) do { _Pragma("unroll") for (int _i = 0; _i < 2; ++_i) \
;         __builtin_amdgcn_global_load_lds((const unsigned*)((const char*)(gbase) + (voff)[_i]), (PG8_LAS unsigned*)(lds + (bufoff) + ldsw + _i * 8192), 16, 0, 0); } while (0)
; #define PG8_LDA(dst, b, h) do { _Pragma("unroll") for (int m = 0; m < 4; ++m) _Pragma("unroll") for (int k = 0; k < 2; ++k) dst[m][k] = *(const PG8_LAS bf16x8*)(lds + PG8_SA(b, h) + aoff + m * 2048 + k * 1024); } while (0)
; #define PG8_LDB(dst, b, h) do { _Pragma("unroll") for (int n = 0; n < 2; ++n) _Pragma("unroll") for (int k = 0; k < 2; ++k) dst[n][k] = *(const PG8_LAS bf16x8*)(lds + PG8_SB(b, h) + boff + n * 2048 + k * 1024); } while (0)
; #define PG8_MMA(ai, bj, At, Bt) do { __builtin_amdgcn_s_setprio(1); _Pragma("unroll") for (int m = 0; m < 4; ++m) _Pragma("unroll") for (int n = 0; n < 2; ++n) _Pragma("unroll") for (int k = 0; k < 2; ++k) \
;         acc[ai][bj][m][n] = __builtin_amdgcn_mfma_f32_16x16x32_bf16(Bt[n][k], At[m][k], acc[ai][bj][m][n], 0, 0, 0); __builtin_amdgcn_s_setprio(0); } while (0)
; #define PG8_WAIT_V(n) asm volatile("s_waitcnt vmcnt(" #n ")" ::: "memory")
; #define PG8_WAIT_L(n) asm volatile("s_waitcnt lgkmcnt(" #n ")" ::: "memory")
; #define PG8_BAR __builtin_amdgcn_s_barrier()
; template <class Epi, class Sched, bool ALIGN_EPI = false, bool SP2 = false>
; __device__ __forceinline__ void gemm_phase(PG8_LAS unsigned char* lds, const Gemm g, const Sched& S, const Epi& E) {
;     ...
;             const char* a1 = cA + (size_t)(t + 1) * kstep;
;             const char* a2 = last ? nA : cA + (size_t)(t + 2) * kstep; const char* b2 = last ? nB : cB + (size_t)(t + 2) * kstep;
;             const char* a3 = a2 + kstep; const char* b3 = b2 + kstep;
;             if (last && has_next) S.a_ready(nxt);
;             if constexpr (SP2) {
;             PG8_LDB(B0, 0, 0); PG8_LDB(B1, 0, 1); PG8_SCHED; PG8_LDA(At, 0, 0); PG8_STAGE(PG8_SA(1, 1), a1 + hstep, voffA);
;             PG8_WAIT_V(8); PG8_WAIT_L(0); PG8_BAR; PG8_MMA(0, 0, At, B0); PG8_MMA(0, 1, At, B1); PG8_BAR; PG8_SCHED;
;             PG8_LDA(At, 0, 1); PG8_STAGE(PG8_SB(0, 0), b2, voffB); PG8_STAGE(PG8_SB(0, 1), b2 + hstep, voffB); PG8_STAGE(PG8_SA(0, 0), a2, voffA);
;             PG8_WAIT_V(8); PG8_WAIT_L(0); PG8_BAR; PG8_MMA(1, 0, At, B0); PG8_MMA(1, 1, At, B1); PG8_BAR; PG8_SCHED;
.LBB0_900:
	ds_read_b128 v[114:117], v218
	ds_read_b128 v[118:121], v218 offset:1024
	ds_read_b128 v[138:141], v218 offset:2048
	ds_read_b128 v[142:145], v218 offset:3072
	ds_read_b128 v[146:149], v219
	ds_read_b128 v[150:153], v219 offset:1024
	ds_read_b128 v[154:157], v219 offset:2048
	ds_read_b128 v[158:161], v219 offset:3072
	s_add_u32 s34, s8, 0xfff80080
	s_addc_u32 s35, s9, -1
	s_cmp_eq_u32 s60, 28
	s_cselect_b32 s37, s19, s35
	s_cselect_b32 s36, s56, s34
	s_cselect_b32 s35, s17, s59
	s_cselect_b32 s34, s57, s58
	v_lshl_add_u64 v[170:171], s[8:9], 0, v[180:181]
	s_add_i32 m0, s27, 0xc000
	ds_read_b128 v[162:165], v220
	ds_read_b128 v[166:169], v220 offset:1024
	ds_read_b128 v[190:193], v220 offset:2048
	ds_read_b128 v[194:197], v220 offset:3072
	ds_read_b128 v[198:201], v220 offset:4096
	ds_read_b128 v[202:205], v220 offset:5120
	ds_read_b128 v[206:209], v220 offset:6144
	ds_read_b128 v[210:213], v220 offset:7168
	global_load_lds_dwordx4 v[170:171], off
	v_lshl_add_u64 v[170:171], s[8:9], 0, v[182:183]
	s_add_i32 m0, s27, 0xe000
	s_nop 0
	global_load_lds_dwordx4 v[170:171], off
	s_waitcnt vmcnt(8)
	s_waitcnt lgkmcnt(0)
	s_barrier
	s_setprio 1
	s_waitcnt lgkmcnt(0)
	v_mfma_f32_16x16x32_bf16 v[134:137], v[114:117], v[162:165], v[134:137]
	v_mfma_f32_16x16x32_bf16 v[130:133], v[138:141], v[162:165], v[130:133]
	v_mfma_f32_16x16x32_bf16 v[126:129], v[114:117], v[190:193], v[126:129]
	v_mfma_f32_16x16x32_bf16 v[122:125], v[138:141], v[190:193], v[122:125]
	v_mfma_f32_16x16x32_bf16 v[110:113], v[114:117], v[198:201], v[110:113]
	v_mfma_f32_16x16x32_bf16 v[106:109], v[138:141], v[198:201], v[106:109]
	v_mfma_f32_16x16x32_bf16 v[102:105], v[114:117], v[206:209], v[102:105]
	v_mfma_f32_16x16x32_bf16 v[98:101], v[138:141], v[206:209], v[98:101]
	v_mfma_f32_16x16x32_bf16 v[134:137], v[118:121], v[166:169], v[134:137]
	v_mfma_f32_16x16x32_bf16 v[130:133], v[142:145], v[166:169], v[130:133]
	v_mfma_f32_16x16x32_bf16 v[126:129], v[118:121], v[194:197], v[126:129]
	v_mfma_f32_16x16x32_bf16 v[122:125], v[142:145], v[194:197], v[122:125]
	v_mfma_f32_16x16x32_bf16 v[110:113], v[118:121], v[202:205], v[110:113]
	v_mfma_f32_16x16x32_bf16 v[106:109], v[142:145], v[202:205], v[106:109]
	v_mfma_f32_16x16x32_bf16 v[102:105], v[118:121], v[210:213], v[102:105]
	v_mfma_f32_16x16x32_bf16 v[98:101], v[142:145], v[210:213], v[98:101]
	s_setprio 0
	s_setprio 1
	v_mfma_f32_16x16x32_bf16 v[62:65], v[146:149], v[162:165], v[62:65]
	v_mfma_f32_16x16x32_bf16 v[58:61], v[154:157], v[162:165], v[58:61]
	v_mfma_f32_16x16x32_bf16 v[54:57], v[146:149], v[190:193], v[54:57]
	v_mfma_f32_16x16x32_bf16 v[50:53], v[154:157], v[190:193], v[50:53]
	v_mfma_f32_16x16x32_bf16 v[46:49], v[146:149], v[198:201], v[46:49]
	v_mfma_f32_16x16x32_bf16 v[42:45], v[154:157], v[198:201], v[42:45]
	v_mfma_f32_16x16x32_bf16 v[38:41], v[146:149], v[206:209], v[38:41]
	v_mfma_f32_16x16x32_bf16 v[34:37], v[154:157], v[206:209], v[34:37]
	v_mfma_f32_16x16x32_bf16 v[62:65], v[150:153], v[166:169], v[62:65]
	v_mfma_f32_16x16x32_bf16 v[58:61], v[158:161], v[166:169], v[58:61]
	v_mfma_f32_16x16x32_bf16 v[54:57], v[150:153], v[194:197], v[54:57]
	v_mfma_f32_16x16x32_bf16 v[50:53], v[158:161], v[194:197], v[50:53]
	v_mfma_f32_16x16x32_bf16 v[46:49], v[150:153], v[202:205], v[46:49]
	v_mfma_f32_16x16x32_bf16 v[42:45], v[158:161], v[202:205], v[42:45]
	v_mfma_f32_16x16x32_bf16 v[38:41], v[150:153], v[210:213], v[38:41]
	v_mfma_f32_16x16x32_bf16 v[34:37], v[158:161], v[210:213], v[34:37]
	s_setprio 0
	s_barrier
	s_add_i32 s61, s54, s40
	v_lshl_add_u64 v[170:171], s[34:35], 0, v[174:175]
	s_mov_b32 m0, s61
	ds_read_b128 v[162:165], v220 offset:16384
	ds_read_b128 v[166:169], v220 offset:17408
	ds_read_b128 v[190:193], v220 offset:18432
	ds_read_b128 v[194:197], v220 offset:19456
	ds_read_b128 v[198:201], v220 offset:20480
	ds_read_b128 v[202:205], v220 offset:21504
	ds_read_b128 v[206:209], v220 offset:22528
	ds_read_b128 v[210:213], v220 offset:23552
	global_load_lds_dwordx4 v[170:171], off
	s_add_i32 m0, s61, 0x2000
	s_add_u32 s62, s34, 0x80000
	v_lshl_add_u64 v[214:215], s[34:35], 0, v[178:179]
	s_addc_u32 s63, s35, 0
	s_add_i32 s61, s55, s40
	global_load_lds_dwordx4 v[214:215], off
	v_lshl_add_u64 v[222:223], s[62:63], 0, v[174:175]
	s_mov_b32 m0, s61
	v_lshl_add_u64 v[224:225], s[36:37], 0, v[176:177]
	global_load_lds_dwordx4 v[222:223], off
	v_lshl_add_u64 v[222:223], s[62:63], 0, v[178:179]
	s_add_i32 m0, s61, 0x2000
	s_nop 0
	global_load_lds_dwordx4 v[222:223], off
	v_lshl_add_u64 v[222:223], s[36:37], 0, v[172:173]
	s_waitcnt vmcnt(6)
	s_waitcnt lgkmcnt(0)
	s_barrier
; #define PG8_STAGE(bufoff, gbase, voff) do { _Pragma("unroll") for (int _i = 0; _i < 2; ++_i) \
;         __builtin_amdgcn_global_load_lds((const unsigned*)((const char*)(gbase) + (voff)[_i]), (PG8_LAS unsigned*)(lds + (bufoff) + ldsw + _i * 8192), 16, 0, 0); } while (0)
; #define PG8_LDA(dst, b, h) do { _Pragma("unroll") for (int m = 0; m < 4; ++m) _Pragma("unroll") for (int k = 0; k < 2; ++k) dst[m][k] = *(const PG8_LAS bf16x8*)(lds + PG8_SA(b, h) + aoff + m * 2048 + k * 1024); } while (0)
; #define PG8_LDB(dst, b, h) do { _Pragma("unroll") for (int n = 0; n < 2; ++n) _Pragma("unroll") for (int k = 0; k < 2; ++k) dst[n][k] = *(const PG8_LAS bf16x8*)(lds + PG8_SB(b, h) + boff + n * 2048 + k * 1024); } while (0)
; #define PG8_MMA(ai, bj, At, Bt) do { __builtin_amdgcn_s_setprio(1); _Pragma("unroll") for (int m = 0; m < 4; ++m) _Pragma("unroll") for (int n = 0; n < 2; ++n) _Pragma("unroll") for (int k = 0; k < 2; ++k) \
;         acc[ai][bj][m][n] = __builtin_amdgcn_mfma_f32_16x16x32_bf16(Bt[n][k], At[m][k], acc[ai][bj][m][n], 0, 0, 0); __builtin_amdgcn_s_setprio(0); } while (0)
; #define PG8_WAIT_V(n) asm volatile("s_waitcnt vmcnt(" #n ")" ::: "memory")
; #define PG8_WAIT_L(n) asm volatile("s_waitcnt lgkmcnt(" #n ")" ::: "memory")
; #define PG8_BAR __builtin_amdgcn_s_barrier()
; #define PG8_SCHED __builtin_amdgcn_sched_barrier(0)
; #define PG8_STAGE(bufoff, gbase, voff) do { _Pragma("unroll") for (int _i = 0; _i < 2; ++_i) \
;         __builtin_amdgcn_global_load_lds((const unsigned*)((const char*)(gbase) + (voff)[_i]), (PG8_LAS unsigned*)(lds + (bufoff) + ldsw + _i * 8192), 16, 0, 0); } while (0)
; #define PG8_WAIT_V(n) asm volatile("s_waitcnt vmcnt(" #n ")" ::: "memory")
; #define PG8_WAIT_L(n) asm volatile("s_waitcnt lgkmcnt(" #n ")" ::: "memory")
; #define PG8_BAR __builtin_amdgcn_s_barrier()
; template <class Epi, class Sched, bool ALIGN_EPI = false, bool SP2 = false>
; __device__ __forceinline__ void gemm_phase(PG8_LAS unsigned char* lds, const Gemm g, const Sched& S, const Epi& E) {
;     ...
;             PG8_WAIT_V(8); PG8_WAIT_L(0); PG8_BAR; PG8_MMA(1, 0, At, B0); PG8_MMA(1, 1, At, B1); PG8_BAR; PG8_SCHED;
;             PG8_LDB(B0, 1, 0); PG8_LDB(B1, 1, 1); PG8_SCHED; PG8_LDA(At, 1, 0); PG8_STAGE(PG8_SA(0, 1), a2 + hstep, voffA);
;             PG8_WAIT_V(8); PG8_WAIT_L(0); PG8_BAR; PG8_MMA(0, 0, At, B0); PG8_MMA(0, 1, At, B1); PG8_BAR; PG8_SCHED;
	s_setprio 1
	s_waitcnt lgkmcnt(0)
	v_mfma_f32_16x16x32_bf16 v[94:97], v[114:117], v[162:165], v[94:97]
	v_mfma_f32_16x16x32_bf16 v[90:93], v[138:141], v[162:165], v[90:93]
	v_mfma_f32_16x16x32_bf16 v[86:89], v[114:117], v[190:193], v[86:89]
	v_mfma_f32_16x16x32_bf16 v[82:85], v[138:141], v[190:193], v[82:85]
	v_mfma_f32_16x16x32_bf16 v[78:81], v[114:117], v[198:201], v[78:81]
	v_mfma_f32_16x16x32_bf16 v[74:77], v[138:141], v[198:201], v[74:77]
	v_mfma_f32_16x16x32_bf16 v[70:73], v[114:117], v[206:209], v[70:73]
	v_mfma_f32_16x16x32_bf16 v[66:69], v[138:141], v[206:209], v[66:69]
	v_mfma_f32_16x16x32_bf16 v[94:97], v[118:121], v[166:169], v[94:97]
	v_mfma_f32_16x16x32_bf16 v[90:93], v[142:145], v[166:169], v[90:93]
	v_mfma_f32_16x16x32_bf16 v[86:89], v[118:121], v[194:197], v[86:89]
	v_mfma_f32_16x16x32_bf16 v[82:85], v[142:145], v[194:197], v[82:85]
	v_mfma_f32_16x16x32_bf16 v[78:81], v[118:121], v[202:205], v[78:81]
	v_mfma_f32_16x16x32_bf16 v[74:77], v[142:145], v[202:205], v[74:77]
	v_mfma_f32_16x16x32_bf16 v[70:73], v[118:121], v[210:213], v[70:73]
	v_mfma_f32_16x16x32_bf16 v[66:69], v[142:145], v[210:213], v[66:69]
	s_mov_b32 m0, s27
	s_nop 0
	global_load_lds_dwordx4 v[222:223], off
	s_mov_b32 m0, s29
	s_nop 0
	global_load_lds_dwordx4 v[224:225], off
	s_setprio 0
	s_setprio 1
	v_mfma_f32_16x16x32_bf16 v[30:33], v[146:149], v[162:165], v[30:33]
	v_mfma_f32_16x16x32_bf16 v[26:29], v[154:157], v[162:165], v[26:29]
	v_mfma_f32_16x16x32_bf16 v[22:25], v[146:149], v[190:193], v[22:25]
	v_mfma_f32_16x16x32_bf16 v[18:21], v[154:157], v[190:193], v[18:21]
	v_mfma_f32_16x16x32_bf16 v[14:17], v[146:149], v[198:201], v[14:17]
	v_mfma_f32_16x16x32_bf16 v[10:13], v[154:157], v[198:201], v[10:13]
	v_mfma_f32_16x16x32_bf16 v[6:9], v[146:149], v[206:209], v[6:9]
	v_mfma_f32_16x16x32_bf16 v[2:5], v[154:157], v[206:209], v[2:5]
	v_mfma_f32_16x16x32_bf16 v[30:33], v[150:153], v[166:169], v[30:33]
	v_mfma_f32_16x16x32_bf16 v[26:29], v[158:161], v[166:169], v[26:29]
	v_mfma_f32_16x16x32_bf16 v[22:25], v[150:153], v[194:197], v[22:25]
	v_mfma_f32_16x16x32_bf16 v[18:21], v[158:161], v[194:197], v[18:21]
	v_mfma_f32_16x16x32_bf16 v[14:17], v[150:153], v[202:205], v[14:17]
	v_mfma_f32_16x16x32_bf16 v[10:13], v[158:161], v[202:205], v[10:13]
	v_mfma_f32_16x16x32_bf16 v[6:9], v[150:153], v[210:213], v[6:9]
	v_mfma_f32_16x16x32_bf16 v[2:5], v[158:161], v[210:213], v[2:5]
	s_setprio 0
	s_barrier
	s_add_i32 s61, 0, 0x18000
	s_add_i32 s62, 0, 0x1c000
	v_add_u32_e32 v142, s61, v217
	v_add_u32_e32 v158, s62, v217
	ds_read_b128 v[114:117], v142
	ds_read_b128 v[118:121], v142 offset:1024
	ds_read_b128 v[138:141], v142 offset:2048
	ds_read_b128 v[142:145], v142 offset:3072
	ds_read_b128 v[146:149], v158
	ds_read_b128 v[150:153], v158 offset:1024
	ds_read_b128 v[154:157], v158 offset:2048
	ds_read_b128 v[158:161], v158 offset:3072
	s_add_u32 s36, s36, 0x80000
	s_addc_u32 s37, s37, 0
	s_mov_b32 m0, s41
	v_lshl_add_u64 v[226:227], s[36:37], 0, v[172:173]
	ds_read_b128 v[162:165], v220 offset:32768
	ds_read_b128 v[166:169], v220 offset:33792
	ds_read_b128 v[190:193], v220 offset:34816
	ds_read_b128 v[194:197], v220 offset:35840
	ds_read_b128 v[198:201], v220 offset:36864
	ds_read_b128 v[202:205], v220 offset:37888
	ds_read_b128 v[206:209], v220 offset:38912
	ds_read_b128 v[210:213], v220 offset:39936
	global_load_lds_dwordx4 v[226:227], off
	v_lshl_add_u64 v[226:227], s[36:37], 0, v[176:177]
	s_mov_b32 m0, s42
	s_nop 0
	global_load_lds_dwordx4 v[226:227], off
	s_waitcnt vmcnt(8)
	s_waitcnt lgkmcnt(0)
	s_barrier
	s_setprio 1
	s_waitcnt lgkmcnt(0)
	v_mfma_f32_16x16x32_bf16 v[134:137], v[114:117], v[162:165], v[134:137]
	v_mfma_f32_16x16x32_bf16 v[130:133], v[138:141], v[162:165], v[130:133]
	v_mfma_f32_16x16x32_bf16 v[126:129], v[114:117], v[190:193], v[126:129]
	v_mfma_f32_16x16x32_bf16 v[122:125], v[138:141], v[190:193], v[122:125]
	v_mfma_f32_16x16x32_bf16 v[110:113], v[114:117], v[198:201], v[110:113]
	v_mfma_f32_16x16x32_bf16 v[106:109], v[138:141], v[198:201], v[106:109]
	v_mfma_f32_16x16x32_bf16 v[102:105], v[114:117], v[206:209], v[102:105]
	v_mfma_f32_16x16x32_bf16 v[98:101], v[138:141], v[206:209], v[98:101]
	v_mfma_f32_16x16x32_bf16 v[134:137], v[118:121], v[166:169], v[134:137]
	v_mfma_f32_16x16x32_bf16 v[130:133], v[142:145], v[166:169], v[130:133]
	v_mfma_f32_16x16x32_bf16 v[126:129], v[118:121], v[194:197], v[126:129]
	v_mfma_f32_16x16x32_bf16 v[122:125], v[142:145], v[194:197], v[122:125]
	v_mfma_f32_16x16x32_bf16 v[110:113], v[118:121], v[202:205], v[110:113]
	v_mfma_f32_16x16x32_bf16 v[106:109], v[142:145], v[202:205], v[106:109]
	v_mfma_f32_16x16x32_bf16 v[102:105], v[118:121], v[210:213], v[102:105]
	v_mfma_f32_16x16x32_bf16 v[98:101], v[142:145], v[210:213], v[98:101]
	s_setprio 0
	s_setprio 1
	v_mfma_f32_16x16x32_bf16 v[62:65], v[146:149], v[162:165], v[62:65]
	v_mfma_f32_16x16x32_bf16 v[58:61], v[154:157], v[162:165], v[58:61]
	v_mfma_f32_16x16x32_bf16 v[54:57], v[146:149], v[190:193], v[54:57]
	v_mfma_f32_16x16x32_bf16 v[50:53], v[154:157], v[190:193], v[50:53]
	v_mfma_f32_16x16x32_bf16 v[46:49], v[146:149], v[198:201], v[46:49]
	v_mfma_f32_16x16x32_bf16 v[42:45], v[154:157], v[198:201], v[42:45]
	v_mfma_f32_16x16x32_bf16 v[38:41], v[146:149], v[206:209], v[38:41]
	v_mfma_f32_16x16x32_bf16 v[34:37], v[154:157], v[206:209], v[34:37]
	v_mfma_f32_16x16x32_bf16 v[62:65], v[150:153], v[166:169], v[62:65]
	v_mfma_f32_16x16x32_bf16 v[58:61], v[158:161], v[166:169], v[58:61]
	v_mfma_f32_16x16x32_bf16 v[54:57], v[150:153], v[194:197], v[54:57]
	v_mfma_f32_16x16x32_bf16 v[50:53], v[158:161], v[194:197], v[50:53]
	v_mfma_f32_16x16x32_bf16 v[46:49], v[150:153], v[202:205], v[46:49]
	v_mfma_f32_16x16x32_bf16 v[42:45], v[158:161], v[202:205], v[42:45]
	v_mfma_f32_16x16x32_bf16 v[38:41], v[150:153], v[210:213], v[38:41]
	v_mfma_f32_16x16x32_bf16 v[34:37], v[158:161], v[210:213], v[34:37]
	s_setprio 0
	s_barrier
; #define PG8_STAGE(bufoff, gbase, voff) do { _Pragma("unroll") for (int _i = 0; _i < 2; ++_i) \
;         __builtin_amdgcn_global_load_lds((const unsigned*)((const char*)(gbase) + (voff)[_i]), (PG8_LAS unsigned*)(lds + (bufoff) + ldsw + _i * 8192), 16, 0, 0); } while (0)
; #define PG8_LDA(dst, b, h) do { _Pragma("unroll") for (int m = 0; m < 4; ++m) _Pragma("unroll") for (int k = 0; k < 2; ++k) dst[m][k] = *(const PG8_LAS bf16x8*)(lds + PG8_SA(b, h) + aoff + m * 2048 + k * 1024); } while (0)
; #define PG8_MMA(ai, bj, At, Bt) do { __builtin_amdgcn_s_setprio(1); _Pragma("unroll") for (int m = 0; m < 4; ++m) _Pragma("unroll") for (int n = 0; n < 2; ++n) _Pragma("unroll") for (int k = 0; k < 2; ++k) \
;         acc[ai][bj][m][n] = __builtin_amdgcn_mfma_f32_16x16x32_bf16(Bt[n][k], At[m][k], acc[ai][bj][m][n], 0, 0, 0); __builtin_amdgcn_s_setprio(0); } while (0)
; #define PG8_WAIT_V(n) asm volatile("s_waitcnt vmcnt(" #n ")" ::: "memory")
; #define PG8_WAIT_L(n) asm volatile("s_waitcnt lgkmcnt(" #n ")" ::: "memory")
; #define PG8_BAR __builtin_amdgcn_s_barrier()
; #define PG8_SCHED __builtin_amdgcn_sched_barrier(0)
; #define PG8_STAGE(bufoff, gbase, voff) do { _Pragma("unroll") for (int _i = 0; _i < 2; ++_i) \
;         __builtin_amdgcn_global_load_lds((const unsigned*)((const char*)(gbase) + (voff)[_i]), (PG8_LAS unsigned*)(lds + (bufoff) + ldsw + _i * 8192), 16, 0, 0); } while (0)
; #define PG8_LDA(dst, b, h) do { _Pragma("unroll") for (int m = 0; m < 4; ++m) _Pragma("unroll") for (int k = 0; k < 2; ++k) dst[m][k] = *(const PG8_LAS bf16x8*)(lds + PG8_SA(b, h) + aoff + m * 2048 + k * 1024); } while (0)
; #define PG8_WAIT_V(n) asm volatile("s_waitcnt vmcnt(" #n ")" ::: "memory")
; #define PG8_WAIT_L(n) asm volatile("s_waitcnt lgkmcnt(" #n ")" ::: "memory")
; #define PG8_BAR __builtin_amdgcn_s_barrier()
; template <class Epi, class Sched, bool ALIGN_EPI = false, bool SP2 = false>
; __device__ __forceinline__ void gemm_phase(PG8_LAS unsigned char* lds, const Gemm g, const Sched& S, const Epi& E) {
;     ...
;             PG8_LDA(At, 1, 1); PG8_STAGE(PG8_SB(1, 0), b3, voffB); PG8_STAGE(PG8_SB(1, 1), b3 + hstep, voffB); PG8_STAGE(PG8_SA(1, 0), a3, voffA);
;             PG8_WAIT_V(8); PG8_WAIT_L(0); PG8_BAR; PG8_MMA(1, 0, At, B0); PG8_MMA(1, 1, At, B1); PG8_BAR; PG8_SCHED;
;     ...
;         if constexpr (ALIGN_EPI) { if (wr == 0) PG8_BAR; }
	s_add_i32 s36, s61, s40
	v_lshl_add_u64 v[170:171], v[170:171], 0, s[10:11]
	s_mov_b32 m0, s36
	ds_read_b128 v[162:165], v220 offset:49152
	ds_read_b128 v[166:169], v220 offset:50176
	ds_read_b128 v[190:193], v220 offset:51200
	ds_read_b128 v[194:197], v220 offset:52224
	ds_read_b128 v[198:201], v220 offset:53248
	ds_read_b128 v[202:205], v220 offset:54272
	ds_read_b128 v[206:209], v220 offset:55296
	ds_read_b128 v[210:213], v220 offset:56320
	global_load_lds_dwordx4 v[170:171], off
	s_add_i32 m0, s36, 0x2000
	s_add_u32 s34, s34, 0x80080
	v_lshl_add_u64 v[170:171], v[214:215], 0, s[10:11]
	s_addc_u32 s35, s35, 0
	s_add_i32 s36, s62, s40
	global_load_lds_dwordx4 v[170:171], off
	v_lshl_add_u64 v[170:171], s[34:35], 0, v[174:175]
	s_mov_b32 m0, s36
	s_nop 0
	global_load_lds_dwordx4 v[170:171], off
	v_lshl_add_u64 v[170:171], s[34:35], 0, v[178:179]
	s_add_i32 m0, s36, 0x2000
	s_nop 0
	global_load_lds_dwordx4 v[170:171], off
	v_lshl_add_u64 v[170:171], v[222:223], 0, s[10:11]
	v_lshl_add_u64 v[228:229], v[224:225], 0, s[10:11]
	s_waitcnt vmcnt(6)
	s_waitcnt lgkmcnt(0)
	s_barrier
	s_setprio 1
	s_waitcnt lgkmcnt(0)
	v_mfma_f32_16x16x32_bf16 v[94:97], v[114:117], v[162:165], v[94:97]
	v_mfma_f32_16x16x32_bf16 v[90:93], v[138:141], v[162:165], v[90:93]
	v_mfma_f32_16x16x32_bf16 v[86:89], v[114:117], v[190:193], v[86:89]
	v_mfma_f32_16x16x32_bf16 v[82:85], v[138:141], v[190:193], v[82:85]
	v_mfma_f32_16x16x32_bf16 v[78:81], v[114:117], v[198:201], v[78:81]
	v_mfma_f32_16x16x32_bf16 v[74:77], v[138:141], v[198:201], v[74:77]
	v_mfma_f32_16x16x32_bf16 v[70:73], v[114:117], v[206:209], v[70:73]
	v_mfma_f32_16x16x32_bf16 v[66:69], v[138:141], v[206:209], v[66:69]
	v_mfma_f32_16x16x32_bf16 v[94:97], v[118:121], v[166:169], v[94:97]
	v_mfma_f32_16x16x32_bf16 v[90:93], v[142:145], v[166:169], v[90:93]
	v_mfma_f32_16x16x32_bf16 v[86:89], v[118:121], v[194:197], v[86:89]
	v_mfma_f32_16x16x32_bf16 v[82:85], v[142:145], v[194:197], v[82:85]
	v_mfma_f32_16x16x32_bf16 v[78:81], v[118:121], v[202:205], v[78:81]
	v_mfma_f32_16x16x32_bf16 v[74:77], v[142:145], v[202:205], v[74:77]
	v_mfma_f32_16x16x32_bf16 v[70:73], v[118:121], v[210:213], v[70:73]
	v_mfma_f32_16x16x32_bf16 v[66:69], v[142:145], v[210:213], v[66:69]
	s_mov_b32 m0, s51
	s_nop 0
	global_load_lds_dwordx4 v[170:171], off
	s_mov_b32 m0, s52
	s_nop 0
	global_load_lds_dwordx4 v[228:229], off
	s_setprio 0
	s_setprio 1
	v_mfma_f32_16x16x32_bf16 v[30:33], v[146:149], v[162:165], v[30:33]
	v_mfma_f32_16x16x32_bf16 v[26:29], v[154:157], v[162:165], v[26:29]
	v_mfma_f32_16x16x32_bf16 v[22:25], v[146:149], v[190:193], v[22:25]
	v_mfma_f32_16x16x32_bf16 v[18:21], v[154:157], v[190:193], v[18:21]
	v_mfma_f32_16x16x32_bf16 v[14:17], v[146:149], v[198:201], v[14:17]
	v_mfma_f32_16x16x32_bf16 v[10:13], v[154:157], v[198:201], v[10:13]
	v_mfma_f32_16x16x32_bf16 v[6:9], v[146:149], v[206:209], v[6:9]
	v_mfma_f32_16x16x32_bf16 v[2:5], v[154:157], v[206:209], v[2:5]
	v_mfma_f32_16x16x32_bf16 v[30:33], v[150:153], v[166:169], v[30:33]
	v_mfma_f32_16x16x32_bf16 v[26:29], v[158:161], v[166:169], v[26:29]
	v_mfma_f32_16x16x32_bf16 v[22:25], v[150:153], v[194:197], v[22:25]
	v_mfma_f32_16x16x32_bf16 v[18:21], v[158:161], v[194:197], v[18:21]
	v_mfma_f32_16x16x32_bf16 v[14:17], v[150:153], v[202:205], v[14:17]
	v_mfma_f32_16x16x32_bf16 v[10:13], v[158:161], v[202:205], v[10:13]
	v_mfma_f32_16x16x32_bf16 v[6:9], v[150:153], v[210:213], v[6:9]
	v_mfma_f32_16x16x32_bf16 v[2:5], v[158:161], v[210:213], v[2:5]
	s_setprio 0
	s_barrier
	s_add_i32 s60, s60, 2
	s_add_u32 s8, s8, 0x100
	s_addc_u32 s9, s9, 0
	s_add_u32 s58, s58, 0x100
	s_addc_u32 s59, s59, 0
	s_cmp_gt_u32 s60, 29
	s_cbranch_scc0 .LBB0_900
	s_and_b64 vcc, exec, s[12:13]
	s_cbranch_vccz .LBB0_903
	s_barrier

; #define PG8_STAGE(bufoff, gbase, voff) do { _Pragma("unroll") for (int _i = 0; _i < 2; ++_i) \
;         __builtin_amdgcn_global_load_lds((const unsigned*)((const char*)(gbase) + (voff)[_i]), (PG8_LAS unsigned*)(lds + (bufoff) + ldsw + _i * 8192), 16, 0, 0); } while (0)
; #define PG8_LDA(dst, b, h) do { _Pragma("unroll") for (int m = 0; m < 4; ++m) _Pragma("unroll") for (int k = 0; k < 2; ++k) dst[m][k] = *(const PG8_LAS bf16x8*)(lds + PG8_SA(b, h) + aoff + m * 2048 + k * 1024); } while (0)
; #define PG8_LDB(dst, b, h) do { _Pragma("unroll") for (int n = 0; n < 2; ++n) _Pragma("unroll") for (int k = 0; k < 2; ++k) dst[n][k] = *(const PG8_LAS bf16x8*)(lds + PG8_SB(b, h) + boff + n * 2048 + k * 1024); } while (0)
; #define PG8_MMA(ai, bj, At, Bt) do { __builtin_amdgcn_s_setprio(1); _Pragma("unroll") for (int m = 0; m < 4; ++m) _Pragma("unroll") for (int n = 0; n < 2; ++n) _Pragma("unroll") for (int k = 0; k < 2; ++k) \
;         acc[ai][bj][m][n] = __builtin_amdgcn_mfma_f32_16x16x32_bf16(Bt[n][k], At[m][k], acc[ai][bj][m][n], 0, 0, 0); __builtin_amdgcn_s_setprio(0); } while (0)
; #define PG8_WAIT_V(n) asm volatile("s_waitcnt vmcnt(" #n ")" ::: "memory")
; #define PG8_WAIT_L(n) asm volatile("s_waitcnt lgkmcnt(" #n ")" ::: "memory")
; #define PG8_BAR __builtin_amdgcn_s_barrier()
; template <class Epi, class Sched, bool ALIGN_EPI = false, bool SP2 = false>
; __device__ __forceinline__ void gemm_phase(PG8_LAS unsigned char* lds, const Gemm g, const Sched& S, const Epi& E) {
;     ...
;             const char* a1 = cA + (size_t)(t + 1) * kstep;
;             const char* a2 = last ? nA : cA + (size_t)(t + 2) * kstep; const char* b2 = last ? nB : cB + (size_t)(t + 2) * kstep;
;             const char* a3 = a2 + kstep; const char* b3 = b2 + kstep;
;             if (last && has_next) S.a_ready(nxt);
;             if constexpr (SP2) {
;             PG8_LDB(B0, 0, 0); PG8_LDB(B1, 0, 1); PG8_SCHED; PG8_LDA(At, 0, 0); PG8_STAGE(PG8_SA(1, 1), a1 + hstep, voffA);
;             PG8_WAIT_V(8); PG8_WAIT_L(0); PG8_BAR; PG8_MMA(0, 0, At, B0); PG8_MMA(0, 1, At, B1); PG8_BAR; PG8_SCHED;
;             PG8_LDA(At, 0, 1); PG8_STAGE(PG8_SB(0, 0), b2, voffB); PG8_STAGE(PG8_SB(0, 1), b2 + hstep, voffB); PG8_STAGE(PG8_SA(0, 0), a2, voffA);
;             PG8_WAIT_V(8); PG8_WAIT_L(0); PG8_BAR; PG8_MMA(1, 0, At, B0); PG8_MMA(1, 1, At, B1); PG8_BAR; PG8_SCHED;
.LBB0_1011:
	ds_read_b128 v[154:157], v150
	ds_read_b128 v[158:161], v150 offset:1024
	ds_read_b128 v[162:165], v150 offset:2048
	ds_read_b128 v[166:169], v150 offset:3072
	ds_read_b128 v[170:173], v151
	ds_read_b128 v[174:177], v151 offset:1024
	ds_read_b128 v[178:181], v151 offset:2048
	ds_read_b128 v[182:185], v151 offset:3072
	s_add_u32 s34, s30, 0xfff80080
	s_addc_u32 s35, s31, -1
	s_cmp_eq_u32 s57, 28
	s_cselect_b32 s37, s23, s35
	s_cselect_b32 s36, s53, s34
	s_cselect_b32 s35, s21, s56
	s_cselect_b32 s34, s54, s55
	v_lshl_add_u64 v[146:147], s[30:31], 0, v[138:139]
	s_add_i32 m0, s29, 0xc000
	ds_read_b128 v[188:191], v152
	ds_read_b128 v[192:195], v152 offset:1024
	ds_read_b128 v[196:199], v152 offset:2048
	ds_read_b128 v[200:203], v152 offset:3072
	ds_read_b128 v[204:207], v152 offset:4096
	ds_read_b128 v[208:211], v152 offset:5120
	ds_read_b128 v[212:215], v152 offset:6144
	ds_read_b128 v[216:219], v152 offset:7168
	global_load_lds_dwordx4 v[146:147], off
	v_lshl_add_u64 v[146:147], s[30:31], 0, v[140:141]
	s_add_i32 m0, s29, 0xe000
	s_nop 0
	global_load_lds_dwordx4 v[146:147], off
	s_waitcnt vmcnt(8)
	s_waitcnt lgkmcnt(0)
	s_barrier
	s_setprio 1
	s_waitcnt lgkmcnt(0)
	v_mfma_f32_16x16x32_bf16 v[126:129], v[154:157], v[188:191], v[126:129]
	v_mfma_f32_16x16x32_bf16 v[122:125], v[162:165], v[188:191], v[122:125]
	v_mfma_f32_16x16x32_bf16 v[118:121], v[154:157], v[196:199], v[118:121]
	v_mfma_f32_16x16x32_bf16 v[110:113], v[162:165], v[196:199], v[110:113]
	v_mfma_f32_16x16x32_bf16 v[102:105], v[154:157], v[204:207], v[102:105]
	v_mfma_f32_16x16x32_bf16 v[94:97], v[162:165], v[204:207], v[94:97]
	v_mfma_f32_16x16x32_bf16 v[86:89], v[154:157], v[212:215], v[86:89]
	v_mfma_f32_16x16x32_bf16 v[78:81], v[162:165], v[212:215], v[78:81]
	v_mfma_f32_16x16x32_bf16 v[126:129], v[158:161], v[192:195], v[126:129]
	v_mfma_f32_16x16x32_bf16 v[122:125], v[166:169], v[192:195], v[122:125]
	v_mfma_f32_16x16x32_bf16 v[118:121], v[158:161], v[200:203], v[118:121]
	v_mfma_f32_16x16x32_bf16 v[110:113], v[166:169], v[200:203], v[110:113]
	v_mfma_f32_16x16x32_bf16 v[102:105], v[158:161], v[208:211], v[102:105]
	v_mfma_f32_16x16x32_bf16 v[94:97], v[166:169], v[208:211], v[94:97]
	v_mfma_f32_16x16x32_bf16 v[86:89], v[158:161], v[216:219], v[86:89]
	v_mfma_f32_16x16x32_bf16 v[78:81], v[166:169], v[216:219], v[78:81]
	s_setprio 0
	s_setprio 1
	v_mfma_f32_16x16x32_bf16 v[114:117], v[170:173], v[188:191], v[114:117]
	v_mfma_f32_16x16x32_bf16 v[106:109], v[178:181], v[188:191], v[106:109]
	v_mfma_f32_16x16x32_bf16 v[98:101], v[170:173], v[196:199], v[98:101]
	v_mfma_f32_16x16x32_bf16 v[90:93], v[178:181], v[196:199], v[90:93]
	v_mfma_f32_16x16x32_bf16 v[82:85], v[170:173], v[204:207], v[82:85]
	v_mfma_f32_16x16x32_bf16 v[74:77], v[178:181], v[204:207], v[74:77]
	v_mfma_f32_16x16x32_bf16 v[70:73], v[170:173], v[212:215], v[70:73]
	v_mfma_f32_16x16x32_bf16 v[66:69], v[178:181], v[212:215], v[66:69]
	v_mfma_f32_16x16x32_bf16 v[114:117], v[174:177], v[192:195], v[114:117]
	v_mfma_f32_16x16x32_bf16 v[106:109], v[182:185], v[192:195], v[106:109]
	v_mfma_f32_16x16x32_bf16 v[98:101], v[174:177], v[200:203], v[98:101]
	v_mfma_f32_16x16x32_bf16 v[90:93], v[182:185], v[200:203], v[90:93]
	v_mfma_f32_16x16x32_bf16 v[82:85], v[174:177], v[208:211], v[82:85]
	v_mfma_f32_16x16x32_bf16 v[74:77], v[182:185], v[208:211], v[74:77]
	v_mfma_f32_16x16x32_bf16 v[70:73], v[174:177], v[216:219], v[70:73]
	v_mfma_f32_16x16x32_bf16 v[66:69], v[182:185], v[216:219], v[66:69]
	s_setprio 0
	s_barrier
	s_add_i32 s58, s46, s39
	v_lshl_add_u64 v[146:147], s[34:35], 0, v[132:133]
	s_mov_b32 m0, s58
	ds_read_b128 v[188:191], v152 offset:16384
	ds_read_b128 v[192:195], v152 offset:17408
	ds_read_b128 v[196:199], v152 offset:18432
	ds_read_b128 v[200:203], v152 offset:19456
	ds_read_b128 v[204:207], v152 offset:20480
	ds_read_b128 v[208:211], v152 offset:21504
	ds_read_b128 v[212:215], v152 offset:22528
	ds_read_b128 v[216:219], v152 offset:23552
	global_load_lds_dwordx4 v[146:147], off
	s_add_i32 m0, s58, 0x2000
	s_add_u32 s58, s34, 0x80000
	v_lshl_add_u64 v[220:221], s[34:35], 0, v[136:137]
	s_addc_u32 s59, s35, 0
	s_add_i32 s60, s47, s39
	global_load_lds_dwordx4 v[220:221], off
	v_lshl_add_u64 v[222:223], s[58:59], 0, v[132:133]
	s_mov_b32 m0, s60
	v_lshl_add_u64 v[224:225], s[36:37], 0, v[134:135]
	global_load_lds_dwordx4 v[222:223], off
	v_lshl_add_u64 v[222:223], s[58:59], 0, v[136:137]
	s_add_i32 m0, s60, 0x2000
	s_nop 0
	global_load_lds_dwordx4 v[222:223], off
	v_lshl_add_u64 v[222:223], s[36:37], 0, v[130:131]
	s_waitcnt vmcnt(6)
	s_waitcnt lgkmcnt(0)
	s_barrier
; #define PG8_STAGE(bufoff, gbase, voff) do { _Pragma("unroll") for (int _i = 0; _i < 2; ++_i) \
;         __builtin_amdgcn_global_load_lds((const unsigned*)((const char*)(gbase) + (voff)[_i]), (PG8_LAS unsigned*)(lds + (bufoff) + ldsw + _i * 8192), 16, 0, 0); } while (0)
; #define PG8_LDA(dst, b, h) do { _Pragma("unroll") for (int m = 0; m < 4; ++m) _Pragma("unroll") for (int k = 0; k < 2; ++k) dst[m][k] = *(const PG8_LAS bf16x8*)(lds + PG8_SA(b, h) + aoff + m * 2048 + k * 1024); } while (0)
; #define PG8_LDB(dst, b, h) do { _Pragma("unroll") for (int n = 0; n < 2; ++n) _Pragma("unroll") for (int k = 0; k < 2; ++k) dst[n][k] = *(const PG8_LAS bf16x8*)(lds + PG8_SB(b, h) + boff + n * 2048 + k * 1024); } while (0)
; #define PG8_MMA(ai, bj, At, Bt) do { __builtin_amdgcn_s_setprio(1); _Pragma("unroll") for (int m = 0; m < 4; ++m) _Pragma("unroll") for (int n = 0; n < 2; ++n) _Pragma("unroll") for (int k = 0; k < 2; ++k) \
;         acc[ai][bj][m][n] = __builtin_amdgcn_mfma_f32_16x16x32_bf16(Bt[n][k], At[m][k], acc[ai][bj][m][n], 0, 0, 0); __builtin_amdgcn_s_setprio(0); } while (0)
; #define PG8_WAIT_V(n) asm volatile("s_waitcnt vmcnt(" #n ")" ::: "memory")
; #define PG8_WAIT_L(n) asm volatile("s_waitcnt lgkmcnt(" #n ")" ::: "memory")
; #define PG8_BAR __builtin_amdgcn_s_barrier()
; #define PG8_SCHED __builtin_amdgcn_sched_barrier(0)
; #define PG8_STAGE(bufoff, gbase, voff) do { _Pragma("unroll") for (int _i = 0; _i < 2; ++_i) \
;         __builtin_amdgcn_global_load_lds((const unsigned*)((const char*)(gbase) + (voff)[_i]), (PG8_LAS unsigned*)(lds + (bufoff) + ldsw + _i * 8192), 16, 0, 0); } while (0)
; #define PG8_WAIT_V(n) asm volatile("s_waitcnt vmcnt(" #n ")" ::: "memory")
; #define PG8_WAIT_L(n) asm volatile("s_waitcnt lgkmcnt(" #n ")" ::: "memory")
; #define PG8_BAR __builtin_amdgcn_s_barrier()
; template <class Epi, class Sched, bool ALIGN_EPI = false, bool SP2 = false>
; __device__ __forceinline__ void gemm_phase(PG8_LAS unsigned char* lds, const Gemm g, const Sched& S, const Epi& E) {
;     ...
;             PG8_WAIT_V(8); PG8_WAIT_L(0); PG8_BAR; PG8_MMA(1, 0, At, B0); PG8_MMA(1, 1, At, B1); PG8_BAR; PG8_SCHED;
;             PG8_LDB(B0, 1, 0); PG8_LDB(B1, 1, 1); PG8_SCHED; PG8_LDA(At, 1, 0); PG8_STAGE(PG8_SA(0, 1), a2 + hstep, voffA);
;             PG8_WAIT_V(8); PG8_WAIT_L(0); PG8_BAR; PG8_MMA(0, 0, At, B0); PG8_MMA(0, 1, At, B1); PG8_BAR; PG8_SCHED;
	s_setprio 1
	s_waitcnt lgkmcnt(0)
	v_mfma_f32_16x16x32_bf16 v[62:65], v[154:157], v[188:191], v[62:65]
	v_mfma_f32_16x16x32_bf16 v[58:61], v[162:165], v[188:191], v[58:61]
	v_mfma_f32_16x16x32_bf16 v[54:57], v[154:157], v[196:199], v[54:57]
	v_mfma_f32_16x16x32_bf16 v[46:49], v[162:165], v[196:199], v[46:49]
	v_mfma_f32_16x16x32_bf16 v[38:41], v[154:157], v[204:207], v[38:41]
	v_mfma_f32_16x16x32_bf16 v[30:33], v[162:165], v[204:207], v[30:33]
	v_mfma_f32_16x16x32_bf16 v[22:25], v[154:157], v[212:215], v[22:25]
	v_mfma_f32_16x16x32_bf16 v[14:17], v[162:165], v[212:215], v[14:17]
	v_mfma_f32_16x16x32_bf16 v[62:65], v[158:161], v[192:195], v[62:65]
	v_mfma_f32_16x16x32_bf16 v[58:61], v[166:169], v[192:195], v[58:61]
	v_mfma_f32_16x16x32_bf16 v[54:57], v[158:161], v[200:203], v[54:57]
	v_mfma_f32_16x16x32_bf16 v[46:49], v[166:169], v[200:203], v[46:49]
	v_mfma_f32_16x16x32_bf16 v[38:41], v[158:161], v[208:211], v[38:41]
	v_mfma_f32_16x16x32_bf16 v[30:33], v[166:169], v[208:211], v[30:33]
	v_mfma_f32_16x16x32_bf16 v[22:25], v[158:161], v[216:219], v[22:25]
	v_mfma_f32_16x16x32_bf16 v[14:17], v[166:169], v[216:219], v[14:17]
	s_mov_b32 m0, s29
	s_nop 0
	global_load_lds_dwordx4 v[222:223], off
	s_mov_b32 m0, s40
	s_nop 0
	global_load_lds_dwordx4 v[224:225], off
	s_setprio 0
	s_setprio 1
	v_mfma_f32_16x16x32_bf16 v[50:53], v[170:173], v[188:191], v[50:53]
	v_mfma_f32_16x16x32_bf16 v[42:45], v[178:181], v[188:191], v[42:45]
	v_mfma_f32_16x16x32_bf16 v[34:37], v[170:173], v[196:199], v[34:37]
	v_mfma_f32_16x16x32_bf16 v[26:29], v[178:181], v[196:199], v[26:29]
	v_mfma_f32_16x16x32_bf16 v[18:21], v[170:173], v[204:207], v[18:21]
	v_mfma_f32_16x16x32_bf16 v[10:13], v[178:181], v[204:207], v[10:13]
	v_mfma_f32_16x16x32_bf16 v[6:9], v[170:173], v[212:215], v[6:9]
	v_mfma_f32_16x16x32_bf16 v[2:5], v[178:181], v[212:215], v[2:5]
	v_mfma_f32_16x16x32_bf16 v[50:53], v[174:177], v[192:195], v[50:53]
	v_mfma_f32_16x16x32_bf16 v[42:45], v[182:185], v[192:195], v[42:45]
	v_mfma_f32_16x16x32_bf16 v[34:37], v[174:177], v[200:203], v[34:37]
	v_mfma_f32_16x16x32_bf16 v[26:29], v[182:185], v[200:203], v[26:29]
	v_mfma_f32_16x16x32_bf16 v[18:21], v[174:177], v[208:211], v[18:21]
	v_mfma_f32_16x16x32_bf16 v[10:13], v[182:185], v[208:211], v[10:13]
	v_mfma_f32_16x16x32_bf16 v[6:9], v[174:177], v[216:219], v[6:9]
	v_mfma_f32_16x16x32_bf16 v[2:5], v[182:185], v[216:219], v[2:5]
	s_setprio 0
	s_barrier
	s_add_i32 s58, 0, 0x18000
	v_add_u32_e32 v153, s58, v148
	s_add_i32 s59, 0, 0x1c000
	ds_read_b128 v[154:157], v153
	ds_read_b128 v[158:161], v153 offset:1024
	ds_read_b128 v[162:165], v153 offset:2048
	ds_read_b128 v[166:169], v153 offset:3072
	v_add_u32_e32 v153, s59, v148
	ds_read_b128 v[170:173], v153
	ds_read_b128 v[174:177], v153 offset:1024
	ds_read_b128 v[178:181], v153 offset:2048
	ds_read_b128 v[182:185], v153 offset:3072
	s_add_u32 s36, s36, 0x80000
	s_addc_u32 s37, s37, 0
	s_mov_b32 m0, s41
	v_lshl_add_u64 v[226:227], s[36:37], 0, v[130:131]
	ds_read_b128 v[188:191], v152 offset:32768
	ds_read_b128 v[192:195], v152 offset:33792
	ds_read_b128 v[196:199], v152 offset:34816
	ds_read_b128 v[200:203], v152 offset:35840
	ds_read_b128 v[204:207], v152 offset:36864
	ds_read_b128 v[208:211], v152 offset:37888
	ds_read_b128 v[212:215], v152 offset:38912
	ds_read_b128 v[216:219], v152 offset:39936
	global_load_lds_dwordx4 v[226:227], off
	v_lshl_add_u64 v[226:227], s[36:37], 0, v[134:135]
	s_mov_b32 m0, s42
	s_nop 0
	global_load_lds_dwordx4 v[226:227], off
	s_waitcnt vmcnt(8)
	s_waitcnt lgkmcnt(0)
	s_barrier
	s_setprio 1
	s_waitcnt lgkmcnt(0)
	v_mfma_f32_16x16x32_bf16 v[126:129], v[154:157], v[188:191], v[126:129]
	v_mfma_f32_16x16x32_bf16 v[122:125], v[162:165], v[188:191], v[122:125]
	v_mfma_f32_16x16x32_bf16 v[118:121], v[154:157], v[196:199], v[118:121]
	v_mfma_f32_16x16x32_bf16 v[110:113], v[162:165], v[196:199], v[110:113]
	v_mfma_f32_16x16x32_bf16 v[102:105], v[154:157], v[204:207], v[102:105]
	v_mfma_f32_16x16x32_bf16 v[94:97], v[162:165], v[204:207], v[94:97]
	v_mfma_f32_16x16x32_bf16 v[86:89], v[154:157], v[212:215], v[86:89]
	v_mfma_f32_16x16x32_bf16 v[78:81], v[162:165], v[212:215], v[78:81]
	v_mfma_f32_16x16x32_bf16 v[126:129], v[158:161], v[192:195], v[126:129]
	v_mfma_f32_16x16x32_bf16 v[122:125], v[166:169], v[192:195], v[122:125]
	v_mfma_f32_16x16x32_bf16 v[118:121], v[158:161], v[200:203], v[118:121]
	v_mfma_f32_16x16x32_bf16 v[110:113], v[166:169], v[200:203], v[110:113]
	v_mfma_f32_16x16x32_bf16 v[102:105], v[158:161], v[208:211], v[102:105]
	v_mfma_f32_16x16x32_bf16 v[94:97], v[166:169], v[208:211], v[94:97]
	v_mfma_f32_16x16x32_bf16 v[86:89], v[158:161], v[216:219], v[86:89]
	v_mfma_f32_16x16x32_bf16 v[78:81], v[166:169], v[216:219], v[78:81]
	s_setprio 0
	s_setprio 1
	v_mfma_f32_16x16x32_bf16 v[114:117], v[170:173], v[188:191], v[114:117]
	v_mfma_f32_16x16x32_bf16 v[106:109], v[178:181], v[188:191], v[106:109]
	v_mfma_f32_16x16x32_bf16 v[98:101], v[170:173], v[196:199], v[98:101]
	v_mfma_f32_16x16x32_bf16 v[90:93], v[178:181], v[196:199], v[90:93]
	v_mfma_f32_16x16x32_bf16 v[82:85], v[170:173], v[204:207], v[82:85]
	v_mfma_f32_16x16x32_bf16 v[74:77], v[178:181], v[204:207], v[74:77]
	v_mfma_f32_16x16x32_bf16 v[70:73], v[170:173], v[212:215], v[70:73]
	v_mfma_f32_16x16x32_bf16 v[66:69], v[178:181], v[212:215], v[66:69]
	v_mfma_f32_16x16x32_bf16 v[114:117], v[174:177], v[192:195], v[114:117]
	v_mfma_f32_16x16x32_bf16 v[106:109], v[182:185], v[192:195], v[106:109]
	v_mfma_f32_16x16x32_bf16 v[98:101], v[174:177], v[200:203], v[98:101]
	v_mfma_f32_16x16x32_bf16 v[90:93], v[182:185], v[200:203], v[90:93]
	v_mfma_f32_16x16x32_bf16 v[82:85], v[174:177], v[208:211], v[82:85]
	v_mfma_f32_16x16x32_bf16 v[74:77], v[182:185], v[208:211], v[74:77]
	v_mfma_f32_16x16x32_bf16 v[70:73], v[174:177], v[216:219], v[70:73]
	v_mfma_f32_16x16x32_bf16 v[66:69], v[182:185], v[216:219], v[66:69]
	s_setprio 0
	s_barrier
; #define PG8_STAGE(bufoff, gbase, voff) do { _Pragma("unroll") for (int _i = 0; _i < 2; ++_i) \
;         __builtin_amdgcn_global_load_lds((const unsigned*)((const char*)(gbase) + (voff)[_i]), (PG8_LAS unsigned*)(lds + (bufoff) + ldsw + _i * 8192), 16, 0, 0); } while (0)
; #define PG8_LDA(dst, b, h) do { _Pragma("unroll") for (int m = 0; m < 4; ++m) _Pragma("unroll") for (int k = 0; k < 2; ++k) dst[m][k] = *(const PG8_LAS bf16x8*)(lds + PG8_SA(b, h) + aoff + m * 2048 + k * 1024); } while (0)
; #define PG8_MMA(ai, bj, At, Bt) do { __builtin_amdgcn_s_setprio(1); _Pragma("unroll") for (int m = 0; m < 4; ++m) _Pragma("unroll") for (int n = 0; n < 2; ++n) _Pragma("unroll") for (int k = 0; k < 2; ++k) \
;         acc[ai][bj][m][n] = __builtin_amdgcn_mfma_f32_16x16x32_bf16(Bt[n][k], At[m][k], acc[ai][bj][m][n], 0, 0, 0); __builtin_amdgcn_s_setprio(0); } while (0)
; #define PG8_WAIT_V(n) asm volatile("s_waitcnt vmcnt(" #n ")" ::: "memory")
; #define PG8_WAIT_L(n) asm volatile("s_waitcnt lgkmcnt(" #n ")" ::: "memory")
; #define PG8_BAR __builtin_amdgcn_s_barrier()
; #define PG8_SCHED __builtin_amdgcn_sched_barrier(0)
; #define PG8_STAGE(bufoff, gbase, voff) do { _Pragma("unroll") for (int _i = 0; _i < 2; ++_i) \
;         __builtin_amdgcn_global_load_lds((const unsigned*)((const char*)(gbase) + (voff)[_i]), (PG8_LAS unsigned*)(lds + (bufoff) + ldsw + _i * 8192), 16, 0, 0); } while (0)
; #define PG8_LDA(dst, b, h) do { _Pragma("unroll") for (int m = 0; m < 4; ++m) _Pragma("unroll") for (int k = 0; k < 2; ++k) dst[m][k] = *(const PG8_LAS bf16x8*)(lds + PG8_SA(b, h) + aoff + m * 2048 + k * 1024); } while (0)
; #define PG8_WAIT_V(n) asm volatile("s_waitcnt vmcnt(" #n ")" ::: "memory")
; #define PG8_WAIT_L(n) asm volatile("s_waitcnt lgkmcnt(" #n ")" ::: "memory")
; #define PG8_BAR __builtin_amdgcn_s_barrier()
; template <class Epi, class Sched, bool ALIGN_EPI = false, bool SP2 = false>
; __device__ __forceinline__ void gemm_phase(PG8_LAS unsigned char* lds, const Gemm g, const Sched& S, const Epi& E) {
;     ...
;             PG8_LDA(At, 1, 1); PG8_STAGE(PG8_SB(1, 0), b3, voffB); PG8_STAGE(PG8_SB(1, 1), b3 + hstep, voffB); PG8_STAGE(PG8_SA(1, 0), a3, voffA);
;             PG8_WAIT_V(8); PG8_WAIT_L(0); PG8_BAR; PG8_MMA(1, 0, At, B0); PG8_MMA(1, 1, At, B1); PG8_BAR; PG8_SCHED;
;     ...
;         if constexpr (ALIGN_EPI) { if (wr == 0) PG8_BAR; }
	s_add_i32 s36, s58, s39
	v_lshl_add_u64 v[146:147], v[146:147], 0, s[10:11]
	s_mov_b32 m0, s36
	ds_read_b128 v[188:191], v152 offset:49152
	ds_read_b128 v[192:195], v152 offset:50176
	ds_read_b128 v[196:199], v152 offset:51200
	ds_read_b128 v[200:203], v152 offset:52224
	ds_read_b128 v[204:207], v152 offset:53248
	ds_read_b128 v[208:211], v152 offset:54272
	ds_read_b128 v[212:215], v152 offset:55296
	ds_read_b128 v[216:219], v152 offset:56320
	global_load_lds_dwordx4 v[146:147], off
	s_add_i32 m0, s36, 0x2000
	s_add_u32 s34, s34, 0x80080
	v_lshl_add_u64 v[146:147], v[220:221], 0, s[10:11]
	s_addc_u32 s35, s35, 0
	s_add_i32 s36, s59, s39
	global_load_lds_dwordx4 v[146:147], off
	v_lshl_add_u64 v[146:147], s[34:35], 0, v[132:133]
	s_mov_b32 m0, s36
	s_nop 0
	global_load_lds_dwordx4 v[146:147], off
	v_lshl_add_u64 v[146:147], s[34:35], 0, v[136:137]
	s_add_i32 m0, s36, 0x2000
	s_nop 0
	global_load_lds_dwordx4 v[146:147], off
	v_lshl_add_u64 v[146:147], v[222:223], 0, s[10:11]
	v_lshl_add_u64 v[228:229], v[224:225], 0, s[10:11]
	s_waitcnt vmcnt(6)
	s_waitcnt lgkmcnt(0)
	s_barrier
	s_setprio 1
	s_waitcnt lgkmcnt(0)
	v_mfma_f32_16x16x32_bf16 v[62:65], v[154:157], v[188:191], v[62:65]
	v_mfma_f32_16x16x32_bf16 v[58:61], v[162:165], v[188:191], v[58:61]
	v_mfma_f32_16x16x32_bf16 v[54:57], v[154:157], v[196:199], v[54:57]
	v_mfma_f32_16x16x32_bf16 v[46:49], v[162:165], v[196:199], v[46:49]
	v_mfma_f32_16x16x32_bf16 v[38:41], v[154:157], v[204:207], v[38:41]
	v_mfma_f32_16x16x32_bf16 v[30:33], v[162:165], v[204:207], v[30:33]
	v_mfma_f32_16x16x32_bf16 v[22:25], v[154:157], v[212:215], v[22:25]
	v_mfma_f32_16x16x32_bf16 v[14:17], v[162:165], v[212:215], v[14:17]
	v_mfma_f32_16x16x32_bf16 v[62:65], v[158:161], v[192:195], v[62:65]
	v_mfma_f32_16x16x32_bf16 v[58:61], v[166:169], v[192:195], v[58:61]
	v_mfma_f32_16x16x32_bf16 v[54:57], v[158:161], v[200:203], v[54:57]
	v_mfma_f32_16x16x32_bf16 v[46:49], v[166:169], v[200:203], v[46:49]
	v_mfma_f32_16x16x32_bf16 v[38:41], v[158:161], v[208:211], v[38:41]
	v_mfma_f32_16x16x32_bf16 v[30:33], v[166:169], v[208:211], v[30:33]
	v_mfma_f32_16x16x32_bf16 v[22:25], v[158:161], v[216:219], v[22:25]
	v_mfma_f32_16x16x32_bf16 v[14:17], v[166:169], v[216:219], v[14:17]
	s_mov_b32 m0, s44
	s_nop 0
	global_load_lds_dwordx4 v[146:147], off
	s_mov_b32 m0, s45
	s_nop 0
	global_load_lds_dwordx4 v[228:229], off
	s_setprio 0
	s_setprio 1
	v_mfma_f32_16x16x32_bf16 v[50:53], v[170:173], v[188:191], v[50:53]
	v_mfma_f32_16x16x32_bf16 v[42:45], v[178:181], v[188:191], v[42:45]
	v_mfma_f32_16x16x32_bf16 v[34:37], v[170:173], v[196:199], v[34:37]
	v_mfma_f32_16x16x32_bf16 v[26:29], v[178:181], v[196:199], v[26:29]
	v_mfma_f32_16x16x32_bf16 v[18:21], v[170:173], v[204:207], v[18:21]
	v_mfma_f32_16x16x32_bf16 v[10:13], v[178:181], v[204:207], v[10:13]
	v_mfma_f32_16x16x32_bf16 v[6:9], v[170:173], v[212:215], v[6:9]
	v_mfma_f32_16x16x32_bf16 v[2:5], v[178:181], v[212:215], v[2:5]
	v_mfma_f32_16x16x32_bf16 v[50:53], v[174:177], v[192:195], v[50:53]
	v_mfma_f32_16x16x32_bf16 v[42:45], v[182:185], v[192:195], v[42:45]
	v_mfma_f32_16x16x32_bf16 v[34:37], v[174:177], v[200:203], v[34:37]
	v_mfma_f32_16x16x32_bf16 v[26:29], v[182:185], v[200:203], v[26:29]
	v_mfma_f32_16x16x32_bf16 v[18:21], v[174:177], v[208:211], v[18:21]
	v_mfma_f32_16x16x32_bf16 v[10:13], v[182:185], v[208:211], v[10:13]
	v_mfma_f32_16x16x32_bf16 v[6:9], v[174:177], v[216:219], v[6:9]
	v_mfma_f32_16x16x32_bf16 v[2:5], v[182:185], v[216:219], v[2:5]
	s_setprio 0
	s_barrier
	s_add_i32 s57, s57, 2
	s_add_u32 s30, s30, 0x100
	s_addc_u32 s31, s31, 0
	s_add_u32 s55, s55, 0x100
	s_addc_u32 s56, s56, 0
	s_cmp_gt_u32 s57, 29
	s_cbranch_scc0 .LBB0_1011
	s_and_b64 vcc, exec, s[12:13]
	s_cbranch_vccz .LBB0_1014
	s_barrier

; #define PG8_STAGE(bufoff, gbase, voff) do { _Pragma("unroll") for (int _i = 0; _i < 2; ++_i) \
;         __builtin_amdgcn_global_load_lds((const unsigned*)((const char*)(gbase) + (voff)[_i]), (PG8_LAS unsigned*)(lds + (bufoff) + ldsw + _i * 8192), 16, 0, 0); } while (0)
; #define PG8_LDA(dst, b, h) do { _Pragma("unroll") for (int m = 0; m < 4; ++m) _Pragma("unroll") for (int k = 0; k < 2; ++k) dst[m][k] = *(const PG8_LAS bf16x8*)(lds + PG8_SA(b, h) + aoff + m * 2048 + k * 1024); } while (0)
; #define PG8_LDB(dst, b, h) do { _Pragma("unroll") for (int n = 0; n < 2; ++n) _Pragma("unroll") for (int k = 0; k < 2; ++k) dst[n][k] = *(const PG8_LAS bf16x8*)(lds + PG8_SB(b, h) + boff + n * 2048 + k * 1024); } while (0)
; #define PG8_MMA(ai, bj, At, Bt) do { __builtin_amdgcn_s_setprio(1); _Pragma("unroll") for (int m = 0; m < 4; ++m) _Pragma("unroll") for (int n = 0; n < 2; ++n) _Pragma("unroll") for (int k = 0; k < 2; ++k) \
;         acc[ai][bj][m][n] = __builtin_amdgcn_mfma_f32_16x16x32_bf16(Bt[n][k], At[m][k], acc[ai][bj][m][n], 0, 0, 0); __builtin_amdgcn_s_setprio(0); } while (0)
; #define PG8_WAIT_V(n) asm volatile("s_waitcnt vmcnt(" #n ")" ::: "memory")
; #define PG8_WAIT_L(n) asm volatile("s_waitcnt lgkmcnt(" #n ")" ::: "memory")
; #define PG8_BAR __builtin_amdgcn_s_barrier()
; template <class Epi, class Sched, bool ALIGN_EPI = false, bool SP2 = false>
; __device__ __forceinline__ void gemm_phase(PG8_LAS unsigned char* lds, const Gemm g, const Sched& S, const Epi& E) {
;     ...
;             const char* a1 = cA + (size_t)(t + 1) * kstep;
;             const char* a2 = last ? nA : cA + (size_t)(t + 2) * kstep; const char* b2 = last ? nB : cB + (size_t)(t + 2) * kstep;
;             const char* a3 = a2 + kstep; const char* b3 = b2 + kstep;
;             if (last && has_next) S.a_ready(nxt);
;             if constexpr (SP2) {
;             PG8_LDB(B0, 0, 0); PG8_LDB(B1, 0, 1); PG8_SCHED; PG8_LDA(At, 0, 0); PG8_STAGE(PG8_SA(1, 1), a1 + hstep, voffA);
;             PG8_WAIT_V(8); PG8_WAIT_L(0); PG8_BAR; PG8_MMA(0, 0, At, B0); PG8_MMA(0, 1, At, B1); PG8_BAR; PG8_SCHED;
;             PG8_LDA(At, 0, 1); PG8_STAGE(PG8_SB(0, 0), b2, voffB); PG8_STAGE(PG8_SB(0, 1), b2 + hstep, voffB); PG8_STAGE(PG8_SA(0, 0), a2, voffA);
;             PG8_WAIT_V(8); PG8_WAIT_L(0); PG8_BAR; PG8_MMA(1, 0, At, B0); PG8_MMA(1, 1, At, B1); PG8_BAR; PG8_SCHED;
.LBB0_1349:
	ds_read_b128 v[152:155], v148
	ds_read_b128 v[156:159], v148 offset:1024
	ds_read_b128 v[160:163], v148 offset:2048
	ds_read_b128 v[164:167], v148 offset:3072
	ds_read_b128 v[168:171], v149
	ds_read_b128 v[172:175], v149 offset:1024
	ds_read_b128 v[176:179], v149 offset:2048
	ds_read_b128 v[180:183], v149 offset:3072
	s_add_u32 s36, s34, 0xfff80080
	s_addc_u32 s37, s35, -1
	s_cmp_eq_u32 s59, 28
	s_cselect_b32 s39, s19, s37
	s_cselect_b32 s38, s55, s36
	s_cselect_b32 s37, s21, s58
	s_cselect_b32 s36, s56, s57
	v_lshl_add_u64 v[144:145], s[34:35], 0, v[138:139]
	s_add_i32 m0, s29, 0xc000
	ds_read_b128 v[188:191], v150
	ds_read_b128 v[192:195], v150 offset:1024
	ds_read_b128 v[196:199], v150 offset:2048
	ds_read_b128 v[200:203], v150 offset:3072
	ds_read_b128 v[204:207], v150 offset:4096
	ds_read_b128 v[208:211], v150 offset:5120
	ds_read_b128 v[212:215], v150 offset:6144
	ds_read_b128 v[216:219], v150 offset:7168
	global_load_lds_dwordx4 v[144:145], off
	v_lshl_add_u64 v[144:145], s[34:35], 0, v[140:141]
	s_add_i32 m0, s29, 0xe000
	s_nop 0
	global_load_lds_dwordx4 v[144:145], off
	s_waitcnt vmcnt(8)
	s_waitcnt lgkmcnt(0)
	s_barrier
	s_setprio 1
	s_waitcnt lgkmcnt(0)
	v_mfma_f32_16x16x32_bf16 v[124:127], v[152:155], v[188:191], v[124:127]
	v_mfma_f32_16x16x32_bf16 v[120:123], v[160:163], v[188:191], v[120:123]
	v_mfma_f32_16x16x32_bf16 v[116:119], v[152:155], v[196:199], v[116:119]
	v_mfma_f32_16x16x32_bf16 v[112:115], v[160:163], v[196:199], v[112:115]
	v_mfma_f32_16x16x32_bf16 v[100:103], v[152:155], v[204:207], v[100:103]
	v_mfma_f32_16x16x32_bf16 v[96:99], v[160:163], v[204:207], v[96:99]
	v_mfma_f32_16x16x32_bf16 v[76:79], v[152:155], v[212:215], v[76:79]
	v_mfma_f32_16x16x32_bf16 v[72:75], v[160:163], v[212:215], v[72:75]
	v_mfma_f32_16x16x32_bf16 v[124:127], v[156:159], v[192:195], v[124:127]
	v_mfma_f32_16x16x32_bf16 v[120:123], v[164:167], v[192:195], v[120:123]
	v_mfma_f32_16x16x32_bf16 v[116:119], v[156:159], v[200:203], v[116:119]
	v_mfma_f32_16x16x32_bf16 v[112:115], v[164:167], v[200:203], v[112:115]
	v_mfma_f32_16x16x32_bf16 v[100:103], v[156:159], v[208:211], v[100:103]
	v_mfma_f32_16x16x32_bf16 v[96:99], v[164:167], v[208:211], v[96:99]
	v_mfma_f32_16x16x32_bf16 v[76:79], v[156:159], v[216:219], v[76:79]
	v_mfma_f32_16x16x32_bf16 v[72:75], v[164:167], v[216:219], v[72:75]
	s_setprio 0
	s_setprio 1
	v_mfma_f32_16x16x32_bf16 v[108:111], v[168:171], v[188:191], v[108:111]
	v_mfma_f32_16x16x32_bf16 v[104:107], v[176:179], v[188:191], v[104:107]
	v_mfma_f32_16x16x32_bf16 v[92:95], v[168:171], v[196:199], v[92:95]
	v_mfma_f32_16x16x32_bf16 v[88:91], v[176:179], v[196:199], v[88:91]
	v_mfma_f32_16x16x32_bf16 v[84:87], v[168:171], v[204:207], v[84:87]
	v_mfma_f32_16x16x32_bf16 v[80:83], v[176:179], v[204:207], v[80:83]
	v_mfma_f32_16x16x32_bf16 v[68:71], v[168:171], v[212:215], v[68:71]
	v_mfma_f32_16x16x32_bf16 v[64:67], v[176:179], v[212:215], v[64:67]
	v_mfma_f32_16x16x32_bf16 v[108:111], v[172:175], v[192:195], v[108:111]
	v_mfma_f32_16x16x32_bf16 v[104:107], v[180:183], v[192:195], v[104:107]
	v_mfma_f32_16x16x32_bf16 v[92:95], v[172:175], v[200:203], v[92:95]
	v_mfma_f32_16x16x32_bf16 v[88:91], v[180:183], v[200:203], v[88:91]
	v_mfma_f32_16x16x32_bf16 v[84:87], v[172:175], v[208:211], v[84:87]
	v_mfma_f32_16x16x32_bf16 v[80:83], v[180:183], v[208:211], v[80:83]
	v_mfma_f32_16x16x32_bf16 v[68:71], v[172:175], v[216:219], v[68:71]
	v_mfma_f32_16x16x32_bf16 v[64:67], v[180:183], v[216:219], v[64:67]
	s_setprio 0
	s_barrier
	s_add_i32 s60, s49, s43
	v_lshl_add_u64 v[144:145], s[36:37], 0, v[132:133]
	s_mov_b32 m0, s60
	ds_read_b128 v[188:191], v150 offset:16384
	ds_read_b128 v[192:195], v150 offset:17408
	ds_read_b128 v[196:199], v150 offset:18432
	ds_read_b128 v[200:203], v150 offset:19456
	ds_read_b128 v[204:207], v150 offset:20480
	ds_read_b128 v[208:211], v150 offset:21504
	ds_read_b128 v[212:215], v150 offset:22528
	ds_read_b128 v[216:219], v150 offset:23552
	global_load_lds_dwordx4 v[144:145], off
	s_add_i32 m0, s60, 0x2000
	s_add_u32 s60, s36, 0x80000
	v_lshl_add_u64 v[184:185], s[36:37], 0, v[128:129]
	s_addc_u32 s61, s37, 0
	s_add_i32 s62, s50, s43
	global_load_lds_dwordx4 v[184:185], off
	v_lshl_add_u64 v[220:221], s[60:61], 0, v[132:133]
	s_mov_b32 m0, s62
	v_lshl_add_u64 v[222:223], s[38:39], 0, v[130:131]
	global_load_lds_dwordx4 v[220:221], off
	v_lshl_add_u64 v[220:221], s[60:61], 0, v[128:129]
	s_add_i32 m0, s62, 0x2000
	s_nop 0
	global_load_lds_dwordx4 v[220:221], off
	v_lshl_add_u64 v[220:221], s[38:39], 0, v[134:135]
	s_waitcnt vmcnt(6)
	s_waitcnt lgkmcnt(0)
	s_barrier
; #define PG8_STAGE(bufoff, gbase, voff) do { _Pragma("unroll") for (int _i = 0; _i < 2; ++_i) \
;         __builtin_amdgcn_global_load_lds((const unsigned*)((const char*)(gbase) + (voff)[_i]), (PG8_LAS unsigned*)(lds + (bufoff) + ldsw + _i * 8192), 16, 0, 0); } while (0)
; #define PG8_LDA(dst, b, h) do { _Pragma("unroll") for (int m = 0; m < 4; ++m) _Pragma("unroll") for (int k = 0; k < 2; ++k) dst[m][k] = *(const PG8_LAS bf16x8*)(lds + PG8_SA(b, h) + aoff + m * 2048 + k * 1024); } while (0)
; #define PG8_LDB(dst, b, h) do { _Pragma("unroll") for (int n = 0; n < 2; ++n) _Pragma("unroll") for (int k = 0; k < 2; ++k) dst[n][k] = *(const PG8_LAS bf16x8*)(lds + PG8_SB(b, h) + boff + n * 2048 + k * 1024); } while (0)
; #define PG8_MMA(ai, bj, At, Bt) do { __builtin_amdgcn_s_setprio(1); _Pragma("unroll") for (int m = 0; m < 4; ++m) _Pragma("unroll") for (int n = 0; n < 2; ++n) _Pragma("unroll") for (int k = 0; k < 2; ++k) \
;         acc[ai][bj][m][n] = __builtin_amdgcn_mfma_f32_16x16x32_bf16(Bt[n][k], At[m][k], acc[ai][bj][m][n], 0, 0, 0); __builtin_amdgcn_s_setprio(0); } while (0)
; #define PG8_WAIT_V(n) asm volatile("s_waitcnt vmcnt(" #n ")" ::: "memory")
; #define PG8_WAIT_L(n) asm volatile("s_waitcnt lgkmcnt(" #n ")" ::: "memory")
; #define PG8_BAR __builtin_amdgcn_s_barrier()
; #define PG8_SCHED __builtin_amdgcn_sched_barrier(0)
; #define PG8_STAGE(bufoff, gbase, voff) do { _Pragma("unroll") for (int _i = 0; _i < 2; ++_i) \
;         __builtin_amdgcn_global_load_lds((const unsigned*)((const char*)(gbase) + (voff)[_i]), (PG8_LAS unsigned*)(lds + (bufoff) + ldsw + _i * 8192), 16, 0, 0); } while (0)
; #define PG8_WAIT_V(n) asm volatile("s_waitcnt vmcnt(" #n ")" ::: "memory")
; #define PG8_WAIT_L(n) asm volatile("s_waitcnt lgkmcnt(" #n ")" ::: "memory")
; #define PG8_BAR __builtin_amdgcn_s_barrier()
; template <class Epi, class Sched, bool ALIGN_EPI = false, bool SP2 = false>
; __device__ __forceinline__ void gemm_phase(PG8_LAS unsigned char* lds, const Gemm g, const Sched& S, const Epi& E) {
;     ...
;             PG8_WAIT_V(8); PG8_WAIT_L(0); PG8_BAR; PG8_MMA(1, 0, At, B0); PG8_MMA(1, 1, At, B1); PG8_BAR; PG8_SCHED;
;             PG8_LDB(B0, 1, 0); PG8_LDB(B1, 1, 1); PG8_SCHED; PG8_LDA(At, 1, 0); PG8_STAGE(PG8_SA(0, 1), a2 + hstep, voffA);
;             PG8_WAIT_V(8); PG8_WAIT_L(0); PG8_BAR; PG8_MMA(0, 0, At, B0); PG8_MMA(0, 1, At, B1); PG8_BAR; PG8_SCHED;
	s_setprio 1
	s_waitcnt lgkmcnt(0)
	v_mfma_f32_16x16x32_bf16 v[60:63], v[152:155], v[188:191], v[60:63]
	v_mfma_f32_16x16x32_bf16 v[56:59], v[160:163], v[188:191], v[56:59]
	v_mfma_f32_16x16x32_bf16 v[52:55], v[152:155], v[196:199], v[52:55]
	v_mfma_f32_16x16x32_bf16 v[44:47], v[160:163], v[196:199], v[44:47]
	v_mfma_f32_16x16x32_bf16 v[36:39], v[152:155], v[204:207], v[36:39]
	v_mfma_f32_16x16x32_bf16 v[28:31], v[160:163], v[204:207], v[28:31]
	v_mfma_f32_16x16x32_bf16 v[20:23], v[152:155], v[212:215], v[20:23]
	v_mfma_f32_16x16x32_bf16 v[12:15], v[160:163], v[212:215], v[12:15]
	v_mfma_f32_16x16x32_bf16 v[60:63], v[156:159], v[192:195], v[60:63]
	v_mfma_f32_16x16x32_bf16 v[56:59], v[164:167], v[192:195], v[56:59]
	v_mfma_f32_16x16x32_bf16 v[52:55], v[156:159], v[200:203], v[52:55]
	v_mfma_f32_16x16x32_bf16 v[44:47], v[164:167], v[200:203], v[44:47]
	v_mfma_f32_16x16x32_bf16 v[36:39], v[156:159], v[208:211], v[36:39]
	v_mfma_f32_16x16x32_bf16 v[28:31], v[164:167], v[208:211], v[28:31]
	v_mfma_f32_16x16x32_bf16 v[20:23], v[156:159], v[216:219], v[20:23]
	v_mfma_f32_16x16x32_bf16 v[12:15], v[164:167], v[216:219], v[12:15]
	s_mov_b32 m0, s29
	s_nop 0
	global_load_lds_dwordx4 v[220:221], off
	s_mov_b32 m0, s31
	s_nop 0
	global_load_lds_dwordx4 v[222:223], off
	s_setprio 0
	s_setprio 1
	v_mfma_f32_16x16x32_bf16 v[48:51], v[168:171], v[188:191], v[48:51]
	v_mfma_f32_16x16x32_bf16 v[40:43], v[176:179], v[188:191], v[40:43]
	v_mfma_f32_16x16x32_bf16 v[32:35], v[168:171], v[196:199], v[32:35]
	v_mfma_f32_16x16x32_bf16 v[24:27], v[176:179], v[196:199], v[24:27]
	v_mfma_f32_16x16x32_bf16 v[16:19], v[168:171], v[204:207], v[16:19]
	v_mfma_f32_16x16x32_bf16 v[8:11], v[176:179], v[204:207], v[8:11]
	v_mfma_f32_16x16x32_bf16 v[4:7], v[168:171], v[212:215], v[4:7]
	v_mfma_f32_16x16x32_bf16 v[0:3], v[176:179], v[212:215], v[0:3]
	v_mfma_f32_16x16x32_bf16 v[48:51], v[172:175], v[192:195], v[48:51]
	v_mfma_f32_16x16x32_bf16 v[40:43], v[180:183], v[192:195], v[40:43]
	v_mfma_f32_16x16x32_bf16 v[32:35], v[172:175], v[200:203], v[32:35]
	v_mfma_f32_16x16x32_bf16 v[24:27], v[180:183], v[200:203], v[24:27]
	v_mfma_f32_16x16x32_bf16 v[16:19], v[172:175], v[208:211], v[16:19]
	v_mfma_f32_16x16x32_bf16 v[8:11], v[180:183], v[208:211], v[8:11]
	v_mfma_f32_16x16x32_bf16 v[4:7], v[172:175], v[216:219], v[4:7]
	v_mfma_f32_16x16x32_bf16 v[0:3], v[180:183], v[216:219], v[0:3]
	s_setprio 0
	s_barrier
	s_add_i32 s60, 0, 0x18000
	v_add_u32_e32 v136, s60, v146
	s_add_i32 s61, 0, 0x1c000
	ds_read_b128 v[152:155], v136
	ds_read_b128 v[156:159], v136 offset:1024
	ds_read_b128 v[160:163], v136 offset:2048
	ds_read_b128 v[164:167], v136 offset:3072
	v_add_u32_e32 v136, s61, v146
	ds_read_b128 v[168:171], v136
	ds_read_b128 v[172:175], v136 offset:1024
	ds_read_b128 v[176:179], v136 offset:2048
	ds_read_b128 v[180:183], v136 offset:3072
	s_add_u32 s38, s38, 0x80000
	s_addc_u32 s39, s39, 0
	s_mov_b32 m0, s44
	v_lshl_add_u64 v[224:225], s[38:39], 0, v[134:135]
	ds_read_b128 v[188:191], v150 offset:32768
	ds_read_b128 v[192:195], v150 offset:33792
	ds_read_b128 v[196:199], v150 offset:34816
	ds_read_b128 v[200:203], v150 offset:35840
	ds_read_b128 v[204:207], v150 offset:36864
	ds_read_b128 v[208:211], v150 offset:37888
	ds_read_b128 v[212:215], v150 offset:38912
	ds_read_b128 v[216:219], v150 offset:39936
	global_load_lds_dwordx4 v[224:225], off
	v_lshl_add_u64 v[224:225], s[38:39], 0, v[130:131]
	s_mov_b32 m0, s45
	s_nop 0
	global_load_lds_dwordx4 v[224:225], off
	s_waitcnt vmcnt(8)
	s_waitcnt lgkmcnt(0)
	s_barrier
	s_setprio 1
	s_waitcnt lgkmcnt(0)
	v_mfma_f32_16x16x32_bf16 v[124:127], v[152:155], v[188:191], v[124:127]
	v_mfma_f32_16x16x32_bf16 v[120:123], v[160:163], v[188:191], v[120:123]
	v_mfma_f32_16x16x32_bf16 v[116:119], v[152:155], v[196:199], v[116:119]
	v_mfma_f32_16x16x32_bf16 v[112:115], v[160:163], v[196:199], v[112:115]
	v_mfma_f32_16x16x32_bf16 v[100:103], v[152:155], v[204:207], v[100:103]
	v_mfma_f32_16x16x32_bf16 v[96:99], v[160:163], v[204:207], v[96:99]
	v_mfma_f32_16x16x32_bf16 v[76:79], v[152:155], v[212:215], v[76:79]
	v_mfma_f32_16x16x32_bf16 v[72:75], v[160:163], v[212:215], v[72:75]
	v_mfma_f32_16x16x32_bf16 v[124:127], v[156:159], v[192:195], v[124:127]
	v_mfma_f32_16x16x32_bf16 v[120:123], v[164:167], v[192:195], v[120:123]
	v_mfma_f32_16x16x32_bf16 v[116:119], v[156:159], v[200:203], v[116:119]
	v_mfma_f32_16x16x32_bf16 v[112:115], v[164:167], v[200:203], v[112:115]
	v_mfma_f32_16x16x32_bf16 v[100:103], v[156:159], v[208:211], v[100:103]
	v_mfma_f32_16x16x32_bf16 v[96:99], v[164:167], v[208:211], v[96:99]
	v_mfma_f32_16x16x32_bf16 v[76:79], v[156:159], v[216:219], v[76:79]
	v_mfma_f32_16x16x32_bf16 v[72:75], v[164:167], v[216:219], v[72:75]
	s_setprio 0
	s_setprio 1
	v_mfma_f32_16x16x32_bf16 v[108:111], v[168:171], v[188:191], v[108:111]
	v_mfma_f32_16x16x32_bf16 v[104:107], v[176:179], v[188:191], v[104:107]
	v_mfma_f32_16x16x32_bf16 v[92:95], v[168:171], v[196:199], v[92:95]
	v_mfma_f32_16x16x32_bf16 v[88:91], v[176:179], v[196:199], v[88:91]
	v_mfma_f32_16x16x32_bf16 v[84:87], v[168:171], v[204:207], v[84:87]
	v_mfma_f32_16x16x32_bf16 v[80:83], v[176:179], v[204:207], v[80:83]
	v_mfma_f32_16x16x32_bf16 v[68:71], v[168:171], v[212:215], v[68:71]
	v_mfma_f32_16x16x32_bf16 v[64:67], v[176:179], v[212:215], v[64:67]
	v_mfma_f32_16x16x32_bf16 v[108:111], v[172:175], v[192:195], v[108:111]
	v_mfma_f32_16x16x32_bf16 v[104:107], v[180:183], v[192:195], v[104:107]
	v_mfma_f32_16x16x32_bf16 v[92:95], v[172:175], v[200:203], v[92:95]
	v_mfma_f32_16x16x32_bf16 v[88:91], v[180:183], v[200:203], v[88:91]
	v_mfma_f32_16x16x32_bf16 v[84:87], v[172:175], v[208:211], v[84:87]
	v_mfma_f32_16x16x32_bf16 v[80:83], v[180:183], v[208:211], v[80:83]
	v_mfma_f32_16x16x32_bf16 v[68:71], v[172:175], v[216:219], v[68:71]
	v_mfma_f32_16x16x32_bf16 v[64:67], v[180:183], v[216:219], v[64:67]
	s_setprio 0
	s_barrier
; #define PG8_STAGE(bufoff, gbase, voff) do { _Pragma("unroll") for (int _i = 0; _i < 2; ++_i) \
;         __builtin_amdgcn_global_load_lds((const unsigned*)((const char*)(gbase) + (voff)[_i]), (PG8_LAS unsigned*)(lds + (bufoff) + ldsw + _i * 8192), 16, 0, 0); } while (0)
; #define PG8_LDA(dst, b, h) do { _Pragma("unroll") for (int m = 0; m < 4; ++m) _Pragma("unroll") for (int k = 0; k < 2; ++k) dst[m][k] = *(const PG8_LAS bf16x8*)(lds + PG8_SA(b, h) + aoff + m * 2048 + k * 1024); } while (0)
; #define PG8_MMA(ai, bj, At, Bt) do { __builtin_amdgcn_s_setprio(1); _Pragma("unroll") for (int m = 0; m < 4; ++m) _Pragma("unroll") for (int n = 0; n < 2; ++n) _Pragma("unroll") for (int k = 0; k < 2; ++k) \
;         acc[ai][bj][m][n] = __builtin_amdgcn_mfma_f32_16x16x32_bf16(Bt[n][k], At[m][k], acc[ai][bj][m][n], 0, 0, 0); __builtin_amdgcn_s_setprio(0); } while (0)
; #define PG8_WAIT_V(n) asm volatile("s_waitcnt vmcnt(" #n ")" ::: "memory")
; #define PG8_WAIT_L(n) asm volatile("s_waitcnt lgkmcnt(" #n ")" ::: "memory")
; #define PG8_BAR __builtin_amdgcn_s_barrier()
; #define PG8_SCHED __builtin_amdgcn_sched_barrier(0)
; #define PG8_STAGE(bufoff, gbase, voff) do { _Pragma("unroll") for (int _i = 0; _i < 2; ++_i) \
;         __builtin_amdgcn_global_load_lds((const unsigned*)((const char*)(gbase) + (voff)[_i]), (PG8_LAS unsigned*)(lds + (bufoff) + ldsw + _i * 8192), 16, 0, 0); } while (0)
; #define PG8_LDA(dst, b, h) do { _Pragma("unroll") for (int m = 0; m < 4; ++m) _Pragma("unroll") for (int k = 0; k < 2; ++k) dst[m][k] = *(const PG8_LAS bf16x8*)(lds + PG8_SA(b, h) + aoff + m * 2048 + k * 1024); } while (0)
; #define PG8_WAIT_V(n) asm volatile("s_waitcnt vmcnt(" #n ")" ::: "memory")
; #define PG8_WAIT_L(n) asm volatile("s_waitcnt lgkmcnt(" #n ")" ::: "memory")
; #define PG8_BAR __builtin_amdgcn_s_barrier()
; template <class Epi, class Sched, bool ALIGN_EPI = false, bool SP2 = false>
; __device__ __forceinline__ void gemm_phase(PG8_LAS unsigned char* lds, const Gemm g, const Sched& S, const Epi& E) {
;     ...
;             PG8_LDA(At, 1, 1); PG8_STAGE(PG8_SB(1, 0), b3, voffB); PG8_STAGE(PG8_SB(1, 1), b3 + hstep, voffB); PG8_STAGE(PG8_SA(1, 0), a3, voffA);
;             PG8_WAIT_V(8); PG8_WAIT_L(0); PG8_BAR; PG8_MMA(1, 0, At, B0); PG8_MMA(1, 1, At, B1); PG8_BAR; PG8_SCHED;
;     ...
;         if constexpr (ALIGN_EPI) { if (wr == 0) PG8_BAR; }
	s_add_i32 s38, s60, s43
	v_lshl_add_u64 v[144:145], v[144:145], 0, s[8:9]
	s_mov_b32 m0, s38
	ds_read_b128 v[188:191], v150 offset:49152
	ds_read_b128 v[192:195], v150 offset:50176
	ds_read_b128 v[196:199], v150 offset:51200
	ds_read_b128 v[200:203], v150 offset:52224
	ds_read_b128 v[204:207], v150 offset:53248
	ds_read_b128 v[208:211], v150 offset:54272
	ds_read_b128 v[212:215], v150 offset:55296
	ds_read_b128 v[216:219], v150 offset:56320
	global_load_lds_dwordx4 v[144:145], off
	s_add_i32 m0, s38, 0x2000
	s_add_u32 s36, s36, 0x80080
	v_lshl_add_u64 v[144:145], v[184:185], 0, s[8:9]
	s_addc_u32 s37, s37, 0
	s_add_i32 s38, s61, s43
	global_load_lds_dwordx4 v[144:145], off
	v_lshl_add_u64 v[144:145], s[36:37], 0, v[132:133]
	s_mov_b32 m0, s38
	s_nop 0
	global_load_lds_dwordx4 v[144:145], off
	v_lshl_add_u64 v[144:145], s[36:37], 0, v[128:129]
	s_add_i32 m0, s38, 0x2000
	s_nop 0
	global_load_lds_dwordx4 v[144:145], off
	v_lshl_add_u64 v[144:145], v[220:221], 0, s[8:9]
	v_lshl_add_u64 v[228:229], v[222:223], 0, s[8:9]
	s_waitcnt vmcnt(6)
	s_waitcnt lgkmcnt(0)
	s_barrier
	s_setprio 1
	s_waitcnt lgkmcnt(0)
	v_mfma_f32_16x16x32_bf16 v[60:63], v[152:155], v[188:191], v[60:63]
	v_mfma_f32_16x16x32_bf16 v[56:59], v[160:163], v[188:191], v[56:59]
	v_mfma_f32_16x16x32_bf16 v[52:55], v[152:155], v[196:199], v[52:55]
	v_mfma_f32_16x16x32_bf16 v[44:47], v[160:163], v[196:199], v[44:47]
	v_mfma_f32_16x16x32_bf16 v[36:39], v[152:155], v[204:207], v[36:39]
	v_mfma_f32_16x16x32_bf16 v[28:31], v[160:163], v[204:207], v[28:31]
	v_mfma_f32_16x16x32_bf16 v[20:23], v[152:155], v[212:215], v[20:23]
	v_mfma_f32_16x16x32_bf16 v[12:15], v[160:163], v[212:215], v[12:15]
	v_mfma_f32_16x16x32_bf16 v[60:63], v[156:159], v[192:195], v[60:63]
	v_mfma_f32_16x16x32_bf16 v[56:59], v[164:167], v[192:195], v[56:59]
	v_mfma_f32_16x16x32_bf16 v[52:55], v[156:159], v[200:203], v[52:55]
	v_mfma_f32_16x16x32_bf16 v[44:47], v[164:167], v[200:203], v[44:47]
	v_mfma_f32_16x16x32_bf16 v[36:39], v[156:159], v[208:211], v[36:39]
	v_mfma_f32_16x16x32_bf16 v[28:31], v[164:167], v[208:211], v[28:31]
	v_mfma_f32_16x16x32_bf16 v[20:23], v[156:159], v[216:219], v[20:23]
	v_mfma_f32_16x16x32_bf16 v[12:15], v[164:167], v[216:219], v[12:15]
	s_mov_b32 m0, s47
	s_nop 0
	global_load_lds_dwordx4 v[144:145], off
	s_mov_b32 m0, s48
	s_nop 0
	global_load_lds_dwordx4 v[228:229], off
	s_setprio 0
	s_setprio 1
	v_mfma_f32_16x16x32_bf16 v[48:51], v[168:171], v[188:191], v[48:51]
	v_mfma_f32_16x16x32_bf16 v[40:43], v[176:179], v[188:191], v[40:43]
	v_mfma_f32_16x16x32_bf16 v[32:35], v[168:171], v[196:199], v[32:35]
	v_mfma_f32_16x16x32_bf16 v[24:27], v[176:179], v[196:199], v[24:27]
	v_mfma_f32_16x16x32_bf16 v[16:19], v[168:171], v[204:207], v[16:19]
	v_mfma_f32_16x16x32_bf16 v[8:11], v[176:179], v[204:207], v[8:11]
	v_mfma_f32_16x16x32_bf16 v[4:7], v[168:171], v[212:215], v[4:7]
	v_mfma_f32_16x16x32_bf16 v[0:3], v[176:179], v[212:215], v[0:3]
	v_mfma_f32_16x16x32_bf16 v[48:51], v[172:175], v[192:195], v[48:51]
	v_mfma_f32_16x16x32_bf16 v[40:43], v[180:183], v[192:195], v[40:43]
	v_mfma_f32_16x16x32_bf16 v[32:35], v[172:175], v[200:203], v[32:35]
	v_mfma_f32_16x16x32_bf16 v[24:27], v[180:183], v[200:203], v[24:27]
	v_mfma_f32_16x16x32_bf16 v[16:19], v[172:175], v[208:211], v[16:19]
	v_mfma_f32_16x16x32_bf16 v[8:11], v[180:183], v[208:211], v[8:11]
	v_mfma_f32_16x16x32_bf16 v[4:7], v[172:175], v[216:219], v[4:7]
	v_mfma_f32_16x16x32_bf16 v[0:3], v[180:183], v[216:219], v[0:3]
	s_setprio 0
	s_barrier
	s_add_i32 s59, s59, 2
	s_add_u32 s34, s34, 0x100
	s_addc_u32 s35, s35, 0
	s_add_u32 s57, s57, 0x100
	s_addc_u32 s58, s58, 0
	s_cmp_gt_u32 s59, 29
	s_cbranch_scc0 .LBB0_1349
	s_and_b64 vcc, exec, s[10:11]
	s_cbranch_vccz .LBB0_1352
	s_barrier
